# counted vmcnt waits in the fp8 expert-weight conversion tile loops (was vmcnt(0) per tile)
# speedup vs baseline: 1.0325x; 1.0071x over previous
; #define LAS __attribute__((address_space(3)))
; DI void f8_load(f32x4 (&v)[4][4], const F8Tile& d, int hb, int lane) {
;     const int nq = lane & 15, kq = lane >> 4;
; #pragma unroll
;     for (int it = 0; it < 4; ++it)
; #pragma unroll
;         for (int j = 0; j < 4; ++j) v[it][j] = __builtin_nontemporal_load((const f32x4*)(d.W + (size_t)(d.k0 + hb * 64 + it * 16 + kq * 4 + j) * d.N + d.n0 + 4 * nq));
; }
; DI void phase_p0(const Args& A, LAS unsigned char* lds, int it0, int it1, int gw, int ngw, int wave, int lane) {
;     ...
;     if (it < it1) {
;         f32x4 ra[4][4], rb[4][4]; LAS unsigned char* sc8 = (LAS unsigned char*)scr;
;         F8Tile d = desc(it);
;         f8_load(ra, d, 0, lane); f8_load(rb, d, 1, lane);
.LBB0_143:
	v_lshrrev_b32_e32 v2, 2, v146
	v_and_b32_e32 v1, 12, v2
	v_or_b32_e32 v186, 0x72, v1
	v_or_b32_e32 v187, 0x73, v2
	v_mov_b32_e32 v135, 0
	v_or_b32_e32 v159, 3, v2
	v_or_b32_e32 v163, 19, v2
	v_or_b32_e32 v167, 35, v2
	v_or_b32_e32 v171, 51, v2
	v_or_b32_e32 v175, 0x43, v2
	v_or_b32_e32 v179, 0x53, v2
	v_or_b32_e32 v183, 0x63, v2
	v_add_u32_e32 v2, s6, v187
	v_add_u32_e32 v4, s6, v186
	s_mov_b32 s5, 0
	v_lshlrev_b32_e32 v3, 2, v0
	v_mul_u32_u24_e32 v134, s18, v2
	v_mul_u32_u24_e32 v4, s18, v4
	v_mov_b32_e32 v5, v135
	v_and_b32_e32 v132, 60, v3
	v_lshl_add_u64 v[2:3], v[134:135], 2, s[8:9]
	s_lshl_b64 s[2:3], s[4:5], 2
	v_lshl_add_u64 v[4:5], v[4:5], 2, s[8:9]
	v_lshl_add_u64 v[2:3], v[2:3], 0, s[2:3]
	v_lshlrev_b32_e32 v134, 2, v132
	v_lshl_add_u64 v[4:5], v[4:5], 0, s[2:3]
	v_or_b32_e32 v182, 0x62, v1
	v_or_b32_e32 v184, 0x70, v1
	v_or_b32_e32 v185, 0x71, v1
	v_lshl_add_u64 v[2:3], v[2:3], 0, v[134:135]
	v_lshl_add_u64 v[4:5], v[4:5], 0, v[134:135]
	global_load_dwordx4 v[10:13], v[2:3], off nt
	global_load_dwordx4 v[14:17], v[4:5], off nt
	v_add_u32_e32 v2, s6, v185
	v_add_u32_e32 v4, s6, v184
	v_add_u32_e32 v18, s6, v183
	v_add_u32_e32 v20, s6, v182
	v_mul_u32_u24_e32 v2, s18, v2
	v_mov_b32_e32 v3, v135
	v_mul_u32_u24_e32 v4, s18, v4
	v_mov_b32_e32 v5, v135
	v_mul_u32_u24_e32 v18, s18, v18
	v_mov_b32_e32 v19, v135
	v_mul_u32_u24_e32 v20, s18, v20
	v_mov_b32_e32 v21, v135
	v_lshl_add_u64 v[2:3], v[2:3], 2, s[8:9]
	v_lshl_add_u64 v[4:5], v[4:5], 2, s[8:9]
	v_lshl_add_u64 v[18:19], v[18:19], 2, s[8:9]
	v_lshl_add_u64 v[20:21], v[20:21], 2, s[8:9]
	v_lshl_add_u64 v[2:3], v[2:3], 0, s[2:3]
	v_lshl_add_u64 v[4:5], v[4:5], 0, s[2:3]
	v_lshl_add_u64 v[18:19], v[18:19], 0, s[2:3]
	v_lshl_add_u64 v[20:21], v[20:21], 0, s[2:3]
	v_or_b32_e32 v178, 0x52, v1
	v_or_b32_e32 v180, 0x60, v1
	v_or_b32_e32 v181, 0x61, v1
	v_lshl_add_u64 v[2:3], v[2:3], 0, v[134:135]
	v_lshl_add_u64 v[6:7], v[4:5], 0, v[134:135]
	v_lshl_add_u64 v[18:19], v[18:19], 0, v[134:135]
	v_lshl_add_u64 v[20:21], v[20:21], 0, v[134:135]
	global_load_dwordx4 v[2:5], v[2:3], off nt
	s_nop 0
	global_load_dwordx4 v[6:9], v[6:7], off nt
	s_nop 0
	global_load_dwordx4 v[26:29], v[18:19], off nt
	global_load_dwordx4 v[30:33], v[20:21], off nt
	v_add_u32_e32 v18, s6, v181
	v_add_u32_e32 v20, s6, v180
	v_add_u32_e32 v34, s6, v179
	v_add_u32_e32 v36, s6, v178
	v_mul_u32_u24_e32 v18, s18, v18
	v_mov_b32_e32 v19, v135
	v_mul_u32_u24_e32 v20, s18, v20
	v_mov_b32_e32 v21, v135
	v_mul_u32_u24_e32 v34, s18, v34
	v_mov_b32_e32 v35, v135
	v_mul_u32_u24_e32 v36, s18, v36
	v_mov_b32_e32 v37, v135
	v_lshl_add_u64 v[18:19], v[18:19], 2, s[8:9]
	v_lshl_add_u64 v[20:21], v[20:21], 2, s[8:9]
	v_lshl_add_u64 v[34:35], v[34:35], 2, s[8:9]
	v_lshl_add_u64 v[36:37], v[36:37], 2, s[8:9]
	v_lshl_add_u64 v[18:19], v[18:19], 0, s[2:3]
	v_lshl_add_u64 v[20:21], v[20:21], 0, s[2:3]
	v_lshl_add_u64 v[34:35], v[34:35], 0, s[2:3]
	v_lshl_add_u64 v[36:37], v[36:37], 0, s[2:3]
	v_or_b32_e32 v174, 0x42, v1
	v_or_b32_e32 v176, 0x50, v1
	v_or_b32_e32 v177, 0x51, v1
	v_lshl_add_u64 v[18:19], v[18:19], 0, v[134:135]
	v_lshl_add_u64 v[22:23], v[20:21], 0, v[134:135]
	v_lshl_add_u64 v[34:35], v[34:35], 0, v[134:135]
	v_lshl_add_u64 v[36:37], v[36:37], 0, v[134:135]
	global_load_dwordx4 v[18:21], v[18:19], off nt
	s_nop 0
	global_load_dwordx4 v[22:25], v[22:23], off nt
	s_nop 0
	global_load_dwordx4 v[42:45], v[34:35], off nt
	global_load_dwordx4 v[46:49], v[36:37], off nt
	v_add_u32_e32 v34, s6, v177
	v_add_u32_e32 v36, s6, v176
	v_add_u32_e32 v50, s6, v175
	v_add_u32_e32 v52, s6, v174
	v_mul_u32_u24_e32 v34, s18, v34
	v_mov_b32_e32 v35, v135
	v_mul_u32_u24_e32 v36, s18, v36
	v_mov_b32_e32 v37, v135
	v_mul_u32_u24_e32 v50, s18, v50
	v_mov_b32_e32 v51, v135
	v_mul_u32_u24_e32 v52, s18, v52
	v_mov_b32_e32 v53, v135
	v_lshl_add_u64 v[34:35], v[34:35], 2, s[8:9]
	v_lshl_add_u64 v[36:37], v[36:37], 2, s[8:9]
	v_lshl_add_u64 v[50:51], v[50:51], 2, s[8:9]
	v_lshl_add_u64 v[52:53], v[52:53], 2, s[8:9]
	v_lshl_add_u64 v[34:35], v[34:35], 0, s[2:3]
	v_lshl_add_u64 v[36:37], v[36:37], 0, s[2:3]
	v_lshl_add_u64 v[50:51], v[50:51], 0, s[2:3]
	v_lshl_add_u64 v[52:53], v[52:53], 0, s[2:3]
	v_or_b32_e32 v170, 50, v1
	v_or_b32_e32 v172, 64, v1
	v_or_b32_e32 v173, 0x41, v1
	v_lshl_add_u64 v[34:35], v[34:35], 0, v[134:135]
	v_lshl_add_u64 v[38:39], v[36:37], 0, v[134:135]
	v_lshl_add_u64 v[50:51], v[50:51], 0, v[134:135]
	v_lshl_add_u64 v[52:53], v[52:53], 0, v[134:135]
	global_load_dwordx4 v[34:37], v[34:35], off nt
	s_nop 0
	global_load_dwordx4 v[38:41], v[38:39], off nt
	s_nop 0
	global_load_dwordx4 v[58:61], v[50:51], off nt
	global_load_dwordx4 v[62:65], v[52:53], off nt
	v_add_u32_e32 v50, s6, v173
	v_add_u32_e32 v52, s6, v172
	v_add_u32_e32 v66, s6, v171
	v_add_u32_e32 v68, s6, v170
	v_mul_u32_u24_e32 v50, s18, v50
	v_mov_b32_e32 v51, v135
	v_mul_u32_u24_e32 v52, s18, v52
	v_mov_b32_e32 v53, v135
	v_mul_u32_u24_e32 v66, s18, v66
	v_mov_b32_e32 v67, v135
	v_mul_u32_u24_e32 v68, s18, v68
	v_mov_b32_e32 v69, v135
	v_lshl_add_u64 v[50:51], v[50:51], 2, s[8:9]
	v_lshl_add_u64 v[52:53], v[52:53], 2, s[8:9]
	v_lshl_add_u64 v[66:67], v[66:67], 2, s[8:9]
	v_lshl_add_u64 v[68:69], v[68:69], 2, s[8:9]
	v_lshl_add_u64 v[50:51], v[50:51], 0, s[2:3]
	v_lshl_add_u64 v[52:53], v[52:53], 0, s[2:3]
	v_lshl_add_u64 v[66:67], v[66:67], 0, s[2:3]
	v_lshl_add_u64 v[68:69], v[68:69], 0, s[2:3]
	v_or_b32_e32 v166, 34, v1
	v_or_b32_e32 v168, 48, v1
	v_or_b32_e32 v169, 49, v1
	v_lshl_add_u64 v[50:51], v[50:51], 0, v[134:135]
	v_lshl_add_u64 v[54:55], v[52:53], 0, v[134:135]
	v_lshl_add_u64 v[66:67], v[66:67], 0, v[134:135]
	v_lshl_add_u64 v[68:69], v[68:69], 0, v[134:135]
	global_load_dwordx4 v[50:53], v[50:51], off nt
	s_nop 0
	global_load_dwordx4 v[54:57], v[54:55], off nt
	s_nop 0
	global_load_dwordx4 v[78:81], v[66:67], off nt
	global_load_dwordx4 v[74:77], v[68:69], off nt
	v_add_u32_e32 v66, s6, v169
	v_add_u32_e32 v68, s6, v168
	s_waitcnt vmcnt(26)
; #define LAS __attribute__((address_space(3)))
; DI void f8_load(f32x4 (&v)[4][4], const F8Tile& d, int hb, int lane) {
;     const int nq = lane & 15, kq = lane >> 4;
; #pragma unroll
;     for (int it = 0; it < 4; ++it)
; #pragma unroll
;         for (int j = 0; j < 4; ++j) v[it][j] = __builtin_nontemporal_load((const f32x4*)(d.W + (size_t)(d.k0 + hb * 64 + it * 16 + kq * 4 + j) * d.N + d.n0 + 4 * nq));
; }
; DI void phase_p0(const Args& A, LAS unsigned char* lds, int it0, int it1, int gw, int ngw, int wave, int lane) {
;     ...
;     if (it < it1) {
;         f32x4 ra[4][4], rb[4][4]; LAS unsigned char* sc8 = (LAS unsigned char*)scr;
;         F8Tile d = desc(it);
;         f8_load(ra, d, 0, lane); f8_load(rb, d, 1, lane);
;         for (; it < it1; it += ngw) {
;             const bool vn = it + ngw < it1; F8Tile dn = d; if (vn) dn = desc(it + ngw);
	v_add_u32_e32 v82, s6, v167
	v_add_u32_e32 v84, s6, v166
	v_mul_u32_u24_e32 v66, s18, v66
	v_mov_b32_e32 v67, v135
	v_mul_u32_u24_e32 v68, s18, v68
	v_mov_b32_e32 v69, v135
	v_mul_u32_u24_e32 v82, s18, v82
	v_mov_b32_e32 v83, v135
	v_mul_u32_u24_e32 v84, s18, v84
	v_mov_b32_e32 v85, v135
	v_lshl_add_u64 v[66:67], v[66:67], 2, s[8:9]
	v_lshl_add_u64 v[68:69], v[68:69], 2, s[8:9]
	v_lshl_add_u64 v[82:83], v[82:83], 2, s[8:9]
	v_lshl_add_u64 v[84:85], v[84:85], 2, s[8:9]
	v_lshl_add_u64 v[66:67], v[66:67], 0, s[2:3]
	v_lshl_add_u64 v[68:69], v[68:69], 0, s[2:3]
	v_lshl_add_u64 v[82:83], v[82:83], 0, s[2:3]
	v_lshl_add_u64 v[84:85], v[84:85], 0, s[2:3]
	v_or_b32_e32 v162, 18, v1
	v_or_b32_e32 v164, 32, v1
	v_or_b32_e32 v165, 33, v1
	v_lshl_add_u64 v[66:67], v[66:67], 0, v[134:135]
	v_lshl_add_u64 v[70:71], v[68:69], 0, v[134:135]
	v_lshl_add_u64 v[82:83], v[82:83], 0, v[134:135]
	v_lshl_add_u64 v[84:85], v[84:85], 0, v[134:135]
	global_load_dwordx4 v[66:69], v[66:67], off nt
	s_nop 0
	global_load_dwordx4 v[70:73], v[70:71], off nt
	s_nop 0
	global_load_dwordx4 v[90:93], v[82:83], off nt
	global_load_dwordx4 v[94:97], v[84:85], off nt
	v_add_u32_e32 v82, s6, v165
	v_add_u32_e32 v84, s6, v164
	v_add_u32_e32 v98, s6, v163
	v_add_u32_e32 v100, s6, v162
	v_mul_u32_u24_e32 v82, s18, v82
	v_mov_b32_e32 v83, v135
	v_mul_u32_u24_e32 v84, s18, v84
	v_mov_b32_e32 v85, v135
	v_mul_u32_u24_e32 v98, s18, v98
	v_mov_b32_e32 v99, v135
	v_mul_u32_u24_e32 v100, s18, v100
	v_mov_b32_e32 v101, v135
	v_lshl_add_u64 v[82:83], v[82:83], 2, s[8:9]
	v_lshl_add_u64 v[84:85], v[84:85], 2, s[8:9]
	v_lshl_add_u64 v[98:99], v[98:99], 2, s[8:9]
	v_lshl_add_u64 v[100:101], v[100:101], 2, s[8:9]
	v_lshl_add_u64 v[82:83], v[82:83], 0, s[2:3]
	v_lshl_add_u64 v[84:85], v[84:85], 0, s[2:3]
	v_lshl_add_u64 v[98:99], v[98:99], 0, s[2:3]
	v_lshl_add_u64 v[100:101], v[100:101], 0, s[2:3]
	v_or_b32_e32 v158, 2, v1
	v_or_b32_e32 v160, 16, v1
	v_or_b32_e32 v161, 17, v1
	v_lshl_add_u64 v[82:83], v[82:83], 0, v[134:135]
	v_lshl_add_u64 v[86:87], v[84:85], 0, v[134:135]
	v_lshl_add_u64 v[98:99], v[98:99], 0, v[134:135]
	v_lshl_add_u64 v[100:101], v[100:101], 0, v[134:135]
	global_load_dwordx4 v[82:85], v[82:83], off nt
	s_nop 0
	global_load_dwordx4 v[86:89], v[86:87], off nt
	s_nop 0
	global_load_dwordx4 v[106:109], v[98:99], off nt
	global_load_dwordx4 v[110:113], v[100:101], off nt
	v_add_u32_e32 v98, s6, v161
	v_add_u32_e32 v100, s6, v160
	v_add_u32_e32 v114, s6, v159
	v_add_u32_e32 v116, s6, v158
	v_mul_u32_u24_e32 v98, s18, v98
	v_mov_b32_e32 v99, v135
	v_mul_u32_u24_e32 v100, s18, v100
	v_mov_b32_e32 v101, v135
	v_mul_u32_u24_e32 v114, s18, v114
	v_mov_b32_e32 v115, v135
	v_mul_u32_u24_e32 v116, s18, v116
	v_mov_b32_e32 v117, v135
	v_lshl_add_u64 v[98:99], v[98:99], 2, s[8:9]
	v_lshl_add_u64 v[100:101], v[100:101], 2, s[8:9]
	v_lshl_add_u64 v[114:115], v[114:115], 2, s[8:9]
	v_lshl_add_u64 v[116:117], v[116:117], 2, s[8:9]
	v_lshl_add_u64 v[98:99], v[98:99], 0, s[2:3]
	v_lshl_add_u64 v[100:101], v[100:101], 0, s[2:3]
	v_lshl_add_u64 v[114:115], v[114:115], 0, s[2:3]
	v_lshl_add_u64 v[116:117], v[116:117], 0, s[2:3]
	v_or_b32_e32 v133, 1, v1
	v_lshl_add_u64 v[98:99], v[98:99], 0, v[134:135]
	v_lshl_add_u64 v[102:103], v[100:101], 0, v[134:135]
	v_lshl_add_u64 v[114:115], v[114:115], 0, v[134:135]
	v_lshl_add_u64 v[116:117], v[116:117], 0, v[134:135]
	global_load_dwordx4 v[98:101], v[98:99], off nt
	s_nop 0
	global_load_dwordx4 v[102:105], v[102:103], off nt
	s_nop 0
	global_load_dwordx4 v[122:125], v[114:115], off nt
	global_load_dwordx4 v[126:129], v[116:117], off nt
	v_add_u32_e32 v114, s6, v133
	v_add_u32_e32 v116, s6, v1
	v_mul_u32_u24_e32 v114, s18, v114
	v_mov_b32_e32 v115, v135
	v_mul_u32_u24_e32 v116, s18, v116
	v_mov_b32_e32 v117, v135
	v_lshl_add_u64 v[114:115], v[114:115], 2, s[8:9]
	v_lshl_add_u64 v[116:117], v[116:117], 2, s[8:9]
	v_lshl_add_u64 v[114:115], v[114:115], 0, s[2:3]
	v_lshl_add_u64 v[116:117], v[116:117], 0, s[2:3]
	v_lshl_add_u64 v[114:115], v[114:115], 0, v[134:135]
	v_lshl_add_u64 v[118:119], v[116:117], 0, v[134:135]
	global_load_dwordx4 v[114:117], v[114:115], off nt
	s_nop 0
	global_load_dwordx4 v[118:121], v[118:119], off nt
	v_readlane_b32 s2, v235, 52
	s_mulk_i32 s2, 0x4200
	v_lshlrev_b32_e32 v137, 4, v0
	s_add_i32 s2, s2, 0
	v_and_b32_e32 v138, 0x70, v137
	v_add_u32_e32 v134, s2, v1
	v_lshrrev_b32_e32 v136, 3, v146
	v_add_u32_e32 v157, s2, v138
	s_lshl_b32 s2, s28, 3
	v_readlane_b32 s12, v235, 54
	v_mov_b32_e32 v131, v135
	v_mul_u32_u24_e32 v156, 0x84, v132
	v_mul_u32_u24_e32 v188, 0x84, v136
	v_readlane_b32 s13, v235, 55
	s_sub_i32 s2, s12, s2
	v_mov_b32_e32 v139, v135
	v_mov_b32_e32 v137, v135
	v_or_b32_e32 v140, 8, v136
	v_mov_b32_e32 v141, v135
	v_or_b32_e32 v142, 16, v136
	v_mov_b32_e32 v143, v135
	v_or_b32_e32 v144, 24, v136
	v_mov_b32_e32 v145, v135
	v_or_b32_e32 v148, 32, v136
	v_mov_b32_e32 v149, v135
	v_or_b32_e32 v150, 40, v136
	v_mov_b32_e32 v151, v135
	v_or_b32_e32 v152, 48, v136
	v_mov_b32_e32 v153, v135
	v_or_b32_e32 v154, 56, v136
	v_mov_b32_e32 v155, v135
	s_addk_i32 s2, 0x6c0
	s_mov_b32 s25, 0xc3e00000
	v_add_u32_e32 v188, v157, v188
	v_mov_b32_e32 v189, 0x43e00000
	v_add_u32_e32 v190, v134, v156
	v_mov_b64_e32 v[156:157], v[130:131]
	s_mov_b32 s19, s24
	s_mov_b64 s[12:13], s[10:11]
	s_waitcnt vmcnt(0)
	s_branch .LBB0_145

; #define LAS __attribute__((address_space(3)))
; DI unsigned pk4_fp8(float a, float b, float c, float d) { unsigned p = 0u; p = __builtin_amdgcn_cvt_pk_fp8_f32(f8clamp(a), f8clamp(b), p, false); p = __builtin_amdgcn_cvt_pk_fp8_f32(f8clamp(c), f8clamp(d), p, true); return p; }
; DI void f8_convert_reload(f32x4 (&v)[4][4], int hb, float sc, LAS unsigned char* scr, bool reload, const F8Tile& dn, int lane) {
;     const int nq = lane & 15, kq = lane >> 4;
; #pragma unroll
;     for (int it = 0; it < 4; ++it) {
; #pragma unroll
;         for (int i = 0; i < 4; ++i) *(LAS unsigned*)(scr + (4 * nq + i) * 132 + hb * 64 + it * 16 + kq * 4) = pk4_fp8(v[it][0][i] * sc, v[it][1][i] * sc, v[it][2][i] * sc, v[it][3][i] * sc);
;         if (reload) {
; #pragma unroll
;             for (int j = 0; j < 4; ++j) v[it][j] = __builtin_nontemporal_load((const f32x4*)(dn.W + (size_t)(dn.k0 + hb * 64 + it * 16 + kq * 4 + j) * dn.N + dn.n0 + 4 * nq)); } }
; }
.LBB0_152:
	s_and_b64 vcc, exec, s[16:17]
	s_cbranch_vccnz .Lcvw1
	s_waitcnt vmcnt(0)
.Lcvw1:
	s_waitcnt vmcnt(28)
	v_mul_f32_e32 v134, 0x42800000, v118
	v_mul_f32_e32 v191, 0x42800000, v114
	v_med3_f32 v134, v134, s25, v189
	v_med3_f32 v191, v191, s25, v189
	v_mov_b32_e32 v193, 0
	v_cvt_pk_fp8_f32 v193, v134, v191
	v_mul_f32_e32 v192, 0x42800000, v126
	v_mul_f32_e32 v134, 0x42800000, v122
	v_med3_f32 v191, v192, s25, v189
	v_med3_f32 v134, v134, s25, v189
	v_cvt_pk_fp8_f32 v193, v191, v134 op_sel:[0,0,1]
	v_mul_f32_e32 v134, 0x42800000, v119
	v_mul_f32_e32 v191, 0x42800000, v115
	v_med3_f32 v134, v134, s25, v189
	v_med3_f32 v191, v191, s25, v189
	v_mov_b32_e32 v194, 0
	v_cvt_pk_fp8_f32 v194, v134, v191
	v_mul_f32_e32 v192, 0x42800000, v127
	v_mul_f32_e32 v134, 0x42800000, v123
	v_med3_f32 v191, v192, s25, v189
	v_med3_f32 v134, v134, s25, v189
	v_cvt_pk_fp8_f32 v194, v191, v134 op_sel:[0,0,1]
	v_mul_f32_e32 v134, 0x42800000, v120
	v_mul_f32_e32 v191, 0x42800000, v116
	v_med3_f32 v134, v134, s25, v189
	v_med3_f32 v191, v191, s25, v189
	v_mov_b32_e32 v195, 0
	v_cvt_pk_fp8_f32 v195, v134, v191
	v_mul_f32_e32 v192, 0x42800000, v128
	v_mul_f32_e32 v134, 0x42800000, v124
	v_med3_f32 v191, v192, s25, v189
	v_med3_f32 v134, v134, s25, v189
	v_cvt_pk_fp8_f32 v195, v191, v134 op_sel:[0,0,1]
	v_mul_f32_e32 v134, 0x42800000, v121
	v_mul_f32_e32 v191, 0x42800000, v117
	v_med3_f32 v134, v134, s25, v189
	v_med3_f32 v191, v191, s25, v189
	v_mov_b32_e32 v196, 0
	v_cvt_pk_fp8_f32 v196, v134, v191
	v_mul_f32_e32 v192, 0x42800000, v129
	v_mul_f32_e32 v134, 0x42800000, v125
	v_med3_f32 v191, v192, s25, v189
	v_med3_f32 v134, v134, s25, v189
	v_cvt_pk_fp8_f32 v196, v191, v134 op_sel:[0,0,1]
	v_cndmask_b32_e64 v134, 0, 1, s[16:17]
	v_cmp_ne_u32_e64 s[2:3], 1, v134
	s_andn2_b64 vcc, exec, s[16:17]
	v_lshlrev_b32_e32 v134, 2, v132
	ds_write2_b32 v190, v193, v194 offset1:33
	ds_write2_b32 v190, v195, v196 offset0:66 offset1:99
	s_cbranch_vccnz .LBB0_154
	v_add_u32_e32 v114, s27, v1
	v_add_u32_e32 v122, s27, v158
	v_ashrrev_i32_e32 v117, 31, v114
	v_mad_u64_u32 v[114:115], s[16:17], v114, s18, 0
	v_ashrrev_i32_e32 v125, 31, v122
	v_mad_u64_u32 v[122:123], s[30:31], v122, s18, 0
	v_mov_b32_e32 v116, v115
	v_mov_b32_e32 v124, v123
	v_mad_u64_u32 v[116:117], s[16:17], v117, s18, v[116:117]
	v_mad_u64_u32 v[124:125], s[30:31], v125, s18, v[124:125]
	v_mov_b32_e32 v115, v116
	v_add_u32_e32 v116, s27, v133
	v_mov_b32_e32 v123, v124
	v_add_u32_e32 v124, s27, v159
	v_ashrrev_i32_e32 v119, 31, v116
	v_mad_u64_u32 v[116:117], s[30:31], v116, s18, 0
	v_ashrrev_i32_e32 v127, 31, v124
	v_mad_u64_u32 v[124:125], s[30:31], v124, s18, 0
	v_mov_b32_e32 v118, v117
	v_mov_b32_e32 v126, v125
	v_mad_u64_u32 v[118:119], s[30:31], v119, s18, v[118:119]
	v_mad_u64_u32 v[126:127], s[30:31], v127, s18, v[126:127]
	s_ashr_i32 s17, s4, 31
	s_mov_b32 s16, s4
	v_mov_b32_e32 v117, v118
	v_mov_b32_e32 v125, v126
	v_lshl_add_u64 v[114:115], v[114:115], 2, s[8:9]
	s_lshl_b64 s[16:17], s[16:17], 2
	v_lshl_add_u64 v[116:117], v[116:117], 2, s[8:9]
	v_lshl_add_u64 v[122:123], v[122:123], 2, s[8:9]
	v_lshl_add_u64 v[124:125], v[124:125], 2, s[8:9]
	v_lshl_add_u64 v[114:115], v[114:115], 0, s[16:17]
	v_lshl_add_u64 v[116:117], v[116:117], 0, s[16:17]
	v_lshl_add_u64 v[122:123], v[122:123], 0, s[16:17]
	v_lshl_add_u64 v[124:125], v[124:125], 0, s[16:17]
	v_lshl_add_u64 v[114:115], v[114:115], 0, v[134:135]
	v_lshl_add_u64 v[116:117], v[116:117], 0, v[134:135]
	v_lshl_add_u64 v[122:123], v[122:123], 0, v[134:135]
	v_lshl_add_u64 v[124:125], v[124:125], 0, v[134:135]
	global_load_dwordx4 v[118:121], v[114:115], off nt
	s_nop 0
	global_load_dwordx4 v[114:117], v[116:117], off nt
	s_nop 0
	global_load_dwordx4 v[126:129], v[122:123], off nt
	s_nop 0
	global_load_dwordx4 v[122:125], v[124:125], off nt
.LBB0_154:
	s_waitcnt vmcnt(28)
	v_mul_f32_e32 v191, 0x42800000, v102
	v_mul_f32_e32 v192, 0x42800000, v98
	v_med3_f32 v191, v191, s25, v189
	v_med3_f32 v192, v192, s25, v189
	v_mov_b32_e32 v194, 0
	v_cvt_pk_fp8_f32 v194, v191, v192
	v_mul_f32_e32 v193, 0x42800000, v110
	v_mul_f32_e32 v191, 0x42800000, v106
	v_med3_f32 v192, v193, s25, v189
	v_med3_f32 v191, v191, s25, v189
	v_cvt_pk_fp8_f32 v194, v192, v191 op_sel:[0,0,1]
	v_mul_f32_e32 v191, 0x42800000, v103
	v_mul_f32_e32 v192, 0x42800000, v99
	v_med3_f32 v191, v191, s25, v189
	v_med3_f32 v192, v192, s25, v189
	v_mov_b32_e32 v195, 0
	v_cvt_pk_fp8_f32 v195, v191, v192
	v_mul_f32_e32 v193, 0x42800000, v111
	v_mul_f32_e32 v191, 0x42800000, v107
	v_med3_f32 v192, v193, s25, v189
	v_med3_f32 v191, v191, s25, v189
	v_cvt_pk_fp8_f32 v195, v192, v191 op_sel:[0,0,1]
	v_mul_f32_e32 v191, 0x42800000, v104
	v_mul_f32_e32 v192, 0x42800000, v100
	v_med3_f32 v191, v191, s25, v189
	v_med3_f32 v192, v192, s25, v189
	v_mov_b32_e32 v196, 0
	v_cvt_pk_fp8_f32 v196, v191, v192
	v_mul_f32_e32 v193, 0x42800000, v112
	v_mul_f32_e32 v191, 0x42800000, v108
	v_med3_f32 v192, v193, s25, v189
	v_med3_f32 v191, v191, s25, v189
	v_cvt_pk_fp8_f32 v196, v192, v191 op_sel:[0,0,1]
	v_mul_f32_e32 v191, 0x42800000, v105
	v_mul_f32_e32 v192, 0x42800000, v101
	v_med3_f32 v191, v191, s25, v189
	v_med3_f32 v192, v192, s25, v189
	v_mov_b32_e32 v197, 0
	v_cvt_pk_fp8_f32 v197, v191, v192
	v_mul_f32_e32 v193, 0x42800000, v113
	v_mul_f32_e32 v191, 0x42800000, v109
	v_med3_f32 v192, v193, s25, v189
	v_med3_f32 v191, v191, s25, v189
	v_cvt_pk_fp8_f32 v197, v192, v191 op_sel:[0,0,1]
	s_and_b64 vcc, exec, s[2:3]
	ds_write2_b32 v190, v194, v195 offset0:4 offset1:37
	ds_write2_b32 v190, v196, v197 offset0:70 offset1:103
	s_cbranch_vccnz .LBB0_156
; #define LAS __attribute__((address_space(3)))
; DI unsigned pk4_fp8(float a, float b, float c, float d) { unsigned p = 0u; p = __builtin_amdgcn_cvt_pk_fp8_f32(f8clamp(a), f8clamp(b), p, false); p = __builtin_amdgcn_cvt_pk_fp8_f32(f8clamp(c), f8clamp(d), p, true); return p; }
; DI void f8_convert_reload(f32x4 (&v)[4][4], int hb, float sc, LAS unsigned char* scr, bool reload, const F8Tile& dn, int lane) {
;     const int nq = lane & 15, kq = lane >> 4;
; #pragma unroll
;     for (int it = 0; it < 4; ++it) {
; #pragma unroll
;         for (int i = 0; i < 4; ++i) *(LAS unsigned*)(scr + (4 * nq + i) * 132 + hb * 64 + it * 16 + kq * 4) = pk4_fp8(v[it][0][i] * sc, v[it][1][i] * sc, v[it][2][i] * sc, v[it][3][i] * sc);
;         if (reload) {
; #pragma unroll
;             for (int j = 0; j < 4; ++j) v[it][j] = __builtin_nontemporal_load((const f32x4*)(dn.W + (size_t)(dn.k0 + hb * 64 + it * 16 + kq * 4 + j) * dn.N + dn.n0 + 4 * nq)); } }
; }
	v_add_u32_e32 v98, s27, v160
	v_add_u32_e32 v106, s27, v162
	v_ashrrev_i32_e32 v101, 31, v98
	v_mad_u64_u32 v[98:99], s[16:17], v98, s18, 0
	v_ashrrev_i32_e32 v109, 31, v106
	v_mad_u64_u32 v[106:107], s[30:31], v106, s18, 0
	v_mov_b32_e32 v100, v99
	v_mov_b32_e32 v108, v107
	v_mad_u64_u32 v[100:101], s[16:17], v101, s18, v[100:101]
	v_mad_u64_u32 v[108:109], s[30:31], v109, s18, v[108:109]
	v_mov_b32_e32 v99, v100
	v_add_u32_e32 v100, s27, v161
	v_mov_b32_e32 v107, v108
	v_add_u32_e32 v108, s27, v163
	v_ashrrev_i32_e32 v103, 31, v100
	v_mad_u64_u32 v[100:101], s[30:31], v100, s18, 0
	v_ashrrev_i32_e32 v111, 31, v108
	v_mad_u64_u32 v[108:109], s[30:31], v108, s18, 0
	v_mov_b32_e32 v102, v101
	v_mov_b32_e32 v110, v109
	v_mad_u64_u32 v[102:103], s[30:31], v103, s18, v[102:103]
	v_mad_u64_u32 v[110:111], s[30:31], v111, s18, v[110:111]
	s_ashr_i32 s17, s4, 31
	s_mov_b32 s16, s4
	v_mov_b32_e32 v101, v102
	v_mov_b32_e32 v109, v110
	v_lshl_add_u64 v[98:99], v[98:99], 2, s[8:9]
	s_lshl_b64 s[16:17], s[16:17], 2
	v_lshl_add_u64 v[100:101], v[100:101], 2, s[8:9]
	v_lshl_add_u64 v[106:107], v[106:107], 2, s[8:9]
	v_lshl_add_u64 v[108:109], v[108:109], 2, s[8:9]
	v_lshl_add_u64 v[98:99], v[98:99], 0, s[16:17]
	v_lshl_add_u64 v[100:101], v[100:101], 0, s[16:17]
	v_lshl_add_u64 v[106:107], v[106:107], 0, s[16:17]
	v_lshl_add_u64 v[108:109], v[108:109], 0, s[16:17]
	v_lshl_add_u64 v[98:99], v[98:99], 0, v[134:135]
	v_lshl_add_u64 v[100:101], v[100:101], 0, v[134:135]
	v_lshl_add_u64 v[106:107], v[106:107], 0, v[134:135]
	v_lshl_add_u64 v[108:109], v[108:109], 0, v[134:135]
	global_load_dwordx4 v[102:105], v[98:99], off nt
	s_nop 0
	global_load_dwordx4 v[98:101], v[100:101], off nt
	s_nop 0
	global_load_dwordx4 v[110:113], v[106:107], off nt
	s_nop 0
	global_load_dwordx4 v[106:109], v[108:109], off nt
.LBB0_156:
	s_waitcnt vmcnt(28)
	v_mul_f32_e32 v191, 0x42800000, v86
	v_mul_f32_e32 v192, 0x42800000, v82
	v_med3_f32 v191, v191, s25, v189
	v_med3_f32 v192, v192, s25, v189
	v_mov_b32_e32 v194, 0
	v_cvt_pk_fp8_f32 v194, v191, v192
	v_mul_f32_e32 v193, 0x42800000, v94
	v_mul_f32_e32 v191, 0x42800000, v90
	v_med3_f32 v192, v193, s25, v189
	v_med3_f32 v191, v191, s25, v189
	v_cvt_pk_fp8_f32 v194, v192, v191 op_sel:[0,0,1]
	v_mul_f32_e32 v191, 0x42800000, v87
	v_mul_f32_e32 v192, 0x42800000, v83
	v_med3_f32 v191, v191, s25, v189
	v_med3_f32 v192, v192, s25, v189
	v_mov_b32_e32 v195, 0
	v_cvt_pk_fp8_f32 v195, v191, v192
	v_mul_f32_e32 v193, 0x42800000, v95
	v_mul_f32_e32 v191, 0x42800000, v91
	v_med3_f32 v192, v193, s25, v189
	v_med3_f32 v191, v191, s25, v189
	v_cvt_pk_fp8_f32 v195, v192, v191 op_sel:[0,0,1]
	v_mul_f32_e32 v191, 0x42800000, v88
	v_mul_f32_e32 v192, 0x42800000, v84
	v_med3_f32 v191, v191, s25, v189
	v_med3_f32 v192, v192, s25, v189
	v_mov_b32_e32 v196, 0
	v_cvt_pk_fp8_f32 v196, v191, v192
	v_mul_f32_e32 v193, 0x42800000, v96
	v_mul_f32_e32 v191, 0x42800000, v92
	v_med3_f32 v192, v193, s25, v189
	v_med3_f32 v191, v191, s25, v189
	v_cvt_pk_fp8_f32 v196, v192, v191 op_sel:[0,0,1]
	v_mul_f32_e32 v191, 0x42800000, v89
	v_mul_f32_e32 v192, 0x42800000, v85
	v_med3_f32 v191, v191, s25, v189
	v_med3_f32 v192, v192, s25, v189
	v_mov_b32_e32 v197, 0
	v_cvt_pk_fp8_f32 v197, v191, v192
	v_mul_f32_e32 v193, 0x42800000, v97
	v_mul_f32_e32 v191, 0x42800000, v93
	v_med3_f32 v192, v193, s25, v189
	v_med3_f32 v191, v191, s25, v189
	v_cvt_pk_fp8_f32 v197, v192, v191 op_sel:[0,0,1]
	s_and_b64 vcc, exec, s[2:3]
	ds_write2_b32 v190, v194, v195 offset0:8 offset1:41
	ds_write2_b32 v190, v196, v197 offset0:74 offset1:107
	s_cbranch_vccnz .LBB0_158
	v_add_u32_e32 v82, s27, v164
	v_add_u32_e32 v90, s27, v166
	v_ashrrev_i32_e32 v85, 31, v82
	v_mad_u64_u32 v[82:83], s[16:17], v82, s18, 0
	v_ashrrev_i32_e32 v93, 31, v90
	v_mad_u64_u32 v[90:91], s[30:31], v90, s18, 0
	v_mov_b32_e32 v84, v83
	v_mov_b32_e32 v92, v91
	v_mad_u64_u32 v[84:85], s[16:17], v85, s18, v[84:85]
	v_mad_u64_u32 v[92:93], s[30:31], v93, s18, v[92:93]
	v_mov_b32_e32 v83, v84
	v_add_u32_e32 v84, s27, v165
	v_mov_b32_e32 v91, v92
	v_add_u32_e32 v92, s27, v167
	v_ashrrev_i32_e32 v87, 31, v84
	v_mad_u64_u32 v[84:85], s[30:31], v84, s18, 0
	v_ashrrev_i32_e32 v95, 31, v92
	v_mad_u64_u32 v[92:93], s[30:31], v92, s18, 0
	v_mov_b32_e32 v86, v85
	v_mov_b32_e32 v94, v93
	v_mad_u64_u32 v[86:87], s[30:31], v87, s18, v[86:87]
	v_mad_u64_u32 v[94:95], s[30:31], v95, s18, v[94:95]
	s_ashr_i32 s17, s4, 31
	s_mov_b32 s16, s4
	v_mov_b32_e32 v85, v86
	v_mov_b32_e32 v93, v94
	v_lshl_add_u64 v[82:83], v[82:83], 2, s[8:9]
	s_lshl_b64 s[16:17], s[16:17], 2
	v_lshl_add_u64 v[84:85], v[84:85], 2, s[8:9]
	v_lshl_add_u64 v[90:91], v[90:91], 2, s[8:9]
	v_lshl_add_u64 v[92:93], v[92:93], 2, s[8:9]
	v_lshl_add_u64 v[82:83], v[82:83], 0, s[16:17]
	v_lshl_add_u64 v[84:85], v[84:85], 0, s[16:17]
	v_lshl_add_u64 v[90:91], v[90:91], 0, s[16:17]
	v_lshl_add_u64 v[92:93], v[92:93], 0, s[16:17]
	v_lshl_add_u64 v[82:83], v[82:83], 0, v[134:135]
	v_lshl_add_u64 v[84:85], v[84:85], 0, v[134:135]
	v_lshl_add_u64 v[90:91], v[90:91], 0, v[134:135]
	v_lshl_add_u64 v[92:93], v[92:93], 0, v[134:135]
	global_load_dwordx4 v[86:89], v[82:83], off nt
	s_nop 0
	global_load_dwordx4 v[82:85], v[84:85], off nt
	s_nop 0
	global_load_dwordx4 v[94:97], v[90:91], off nt
	s_nop 0
	global_load_dwordx4 v[90:93], v[92:93], off nt
; #define LAS __attribute__((address_space(3)))
; DI unsigned pk4_fp8(float a, float b, float c, float d) { unsigned p = 0u; p = __builtin_amdgcn_cvt_pk_fp8_f32(f8clamp(a), f8clamp(b), p, false); p = __builtin_amdgcn_cvt_pk_fp8_f32(f8clamp(c), f8clamp(d), p, true); return p; }
; DI void f8_convert_reload(f32x4 (&v)[4][4], int hb, float sc, LAS unsigned char* scr, bool reload, const F8Tile& dn, int lane) {
;     const int nq = lane & 15, kq = lane >> 4;
; #pragma unroll
;     for (int it = 0; it < 4; ++it) {
; #pragma unroll
;         for (int i = 0; i < 4; ++i) *(LAS unsigned*)(scr + (4 * nq + i) * 132 + hb * 64 + it * 16 + kq * 4) = pk4_fp8(v[it][0][i] * sc, v[it][1][i] * sc, v[it][2][i] * sc, v[it][3][i] * sc);
;         if (reload) {
; #pragma unroll
;             for (int j = 0; j < 4; ++j) v[it][j] = __builtin_nontemporal_load((const f32x4*)(dn.W + (size_t)(dn.k0 + hb * 64 + it * 16 + kq * 4 + j) * dn.N + dn.n0 + 4 * nq)); } }
; }
.LBB0_158:
	s_waitcnt vmcnt(28)
	v_mul_f32_e32 v191, 0x42800000, v70
	v_mul_f32_e32 v192, 0x42800000, v66
	v_med3_f32 v191, v191, s25, v189
	v_med3_f32 v192, v192, s25, v189
	v_mov_b32_e32 v194, 0
	v_cvt_pk_fp8_f32 v194, v191, v192
	v_mul_f32_e32 v193, 0x42800000, v74
	v_mul_f32_e32 v191, 0x42800000, v78
	v_med3_f32 v192, v193, s25, v189
	v_med3_f32 v191, v191, s25, v189
	v_cvt_pk_fp8_f32 v194, v192, v191 op_sel:[0,0,1]
	v_mul_f32_e32 v191, 0x42800000, v71
	v_mul_f32_e32 v192, 0x42800000, v67
	v_med3_f32 v191, v191, s25, v189
	v_med3_f32 v192, v192, s25, v189
	v_mov_b32_e32 v195, 0
	v_cvt_pk_fp8_f32 v195, v191, v192
	v_mul_f32_e32 v193, 0x42800000, v75
	v_mul_f32_e32 v191, 0x42800000, v79
	v_med3_f32 v192, v193, s25, v189
	v_med3_f32 v191, v191, s25, v189
	v_cvt_pk_fp8_f32 v195, v192, v191 op_sel:[0,0,1]
	v_mul_f32_e32 v191, 0x42800000, v72
	v_mul_f32_e32 v192, 0x42800000, v68
	v_med3_f32 v191, v191, s25, v189
	v_med3_f32 v192, v192, s25, v189
	v_mov_b32_e32 v196, 0
	v_cvt_pk_fp8_f32 v196, v191, v192
	v_mul_f32_e32 v193, 0x42800000, v76
	v_mul_f32_e32 v191, 0x42800000, v80
	v_med3_f32 v192, v193, s25, v189
	v_med3_f32 v191, v191, s25, v189
	v_cvt_pk_fp8_f32 v196, v192, v191 op_sel:[0,0,1]
	v_mul_f32_e32 v191, 0x42800000, v73
	v_mul_f32_e32 v192, 0x42800000, v69
	v_med3_f32 v191, v191, s25, v189
	v_med3_f32 v192, v192, s25, v189
	v_mov_b32_e32 v197, 0
	v_cvt_pk_fp8_f32 v197, v191, v192
	v_mul_f32_e32 v193, 0x42800000, v77
	v_mul_f32_e32 v191, 0x42800000, v81
	v_med3_f32 v192, v193, s25, v189
	v_med3_f32 v191, v191, s25, v189
	v_cvt_pk_fp8_f32 v197, v192, v191 op_sel:[0,0,1]
	s_and_b64 vcc, exec, s[2:3]
	ds_write2_b32 v190, v194, v195 offset0:12 offset1:45
	ds_write2_b32 v190, v196, v197 offset0:78 offset1:111
	s_cbranch_vccnz .LBB0_160
	v_add_u32_e32 v66, s27, v168
	v_add_u32_e32 v74, s27, v170
	v_ashrrev_i32_e32 v69, 31, v66
	v_mad_u64_u32 v[66:67], s[16:17], v66, s18, 0
	v_ashrrev_i32_e32 v77, 31, v74
	v_mad_u64_u32 v[74:75], s[30:31], v74, s18, 0
	v_mov_b32_e32 v68, v67
	v_mov_b32_e32 v76, v75
	v_mad_u64_u32 v[68:69], s[16:17], v69, s18, v[68:69]
	v_mad_u64_u32 v[76:77], s[30:31], v77, s18, v[76:77]
	v_mov_b32_e32 v67, v68
	v_add_u32_e32 v68, s27, v169
	v_mov_b32_e32 v75, v76
	v_add_u32_e32 v76, s27, v171
	v_ashrrev_i32_e32 v71, 31, v68
	v_mad_u64_u32 v[68:69], s[30:31], v68, s18, 0
	v_ashrrev_i32_e32 v79, 31, v76
	v_mad_u64_u32 v[76:77], s[30:31], v76, s18, 0
	v_mov_b32_e32 v70, v69
	v_mov_b32_e32 v78, v77
	v_mad_u64_u32 v[70:71], s[30:31], v71, s18, v[70:71]
	v_mad_u64_u32 v[78:79], s[30:31], v79, s18, v[78:79]
	s_ashr_i32 s17, s4, 31
	s_mov_b32 s16, s4
	v_mov_b32_e32 v69, v70
	v_mov_b32_e32 v77, v78
	v_lshl_add_u64 v[66:67], v[66:67], 2, s[8:9]
	s_lshl_b64 s[16:17], s[16:17], 2
	v_lshl_add_u64 v[68:69], v[68:69], 2, s[8:9]
	v_lshl_add_u64 v[74:75], v[74:75], 2, s[8:9]
	v_lshl_add_u64 v[76:77], v[76:77], 2, s[8:9]
	v_lshl_add_u64 v[66:67], v[66:67], 0, s[16:17]
	v_lshl_add_u64 v[68:69], v[68:69], 0, s[16:17]
	v_lshl_add_u64 v[74:75], v[74:75], 0, s[16:17]
	v_lshl_add_u64 v[76:77], v[76:77], 0, s[16:17]
	v_lshl_add_u64 v[66:67], v[66:67], 0, v[134:135]
	v_lshl_add_u64 v[68:69], v[68:69], 0, v[134:135]
	v_lshl_add_u64 v[74:75], v[74:75], 0, v[134:135]
	v_lshl_add_u64 v[78:79], v[76:77], 0, v[134:135]
	global_load_dwordx4 v[70:73], v[66:67], off nt
	s_nop 0
	global_load_dwordx4 v[66:69], v[68:69], off nt
	s_nop 0
	global_load_dwordx4 v[74:77], v[74:75], off nt
	s_nop 0
	global_load_dwordx4 v[78:81], v[78:79], off nt
.LBB0_160:
	s_waitcnt vmcnt(28)
	v_mul_f32_e32 v191, 0x42800000, v54
	v_mul_f32_e32 v192, 0x42800000, v50
	v_med3_f32 v191, v191, s25, v189
	v_med3_f32 v192, v192, s25, v189
	v_mov_b32_e32 v194, 0
	v_cvt_pk_fp8_f32 v194, v191, v192
	v_mul_f32_e32 v193, 0x42800000, v62
	v_mul_f32_e32 v191, 0x42800000, v58
	v_med3_f32 v192, v193, s25, v189
	v_med3_f32 v191, v191, s25, v189
	v_cvt_pk_fp8_f32 v194, v192, v191 op_sel:[0,0,1]
	v_mul_f32_e32 v191, 0x42800000, v55
	v_mul_f32_e32 v192, 0x42800000, v51
	v_med3_f32 v191, v191, s25, v189
	v_med3_f32 v192, v192, s25, v189
	v_mov_b32_e32 v195, 0
	v_cvt_pk_fp8_f32 v195, v191, v192
	v_mul_f32_e32 v193, 0x42800000, v63
	v_mul_f32_e32 v191, 0x42800000, v59
	v_med3_f32 v192, v193, s25, v189
	v_med3_f32 v191, v191, s25, v189
	v_cvt_pk_fp8_f32 v195, v192, v191 op_sel:[0,0,1]
	v_mul_f32_e32 v191, 0x42800000, v56
	v_mul_f32_e32 v192, 0x42800000, v52
	v_med3_f32 v191, v191, s25, v189
	v_med3_f32 v192, v192, s25, v189
	v_mov_b32_e32 v196, 0
	v_cvt_pk_fp8_f32 v196, v191, v192
	v_mul_f32_e32 v193, 0x42800000, v64
	v_mul_f32_e32 v191, 0x42800000, v60
	v_med3_f32 v192, v193, s25, v189
	v_med3_f32 v191, v191, s25, v189
	v_cvt_pk_fp8_f32 v196, v192, v191 op_sel:[0,0,1]
	v_mul_f32_e32 v191, 0x42800000, v57
	v_mul_f32_e32 v192, 0x42800000, v53
	v_med3_f32 v191, v191, s25, v189
	v_med3_f32 v192, v192, s25, v189
	v_mov_b32_e32 v197, 0
	v_cvt_pk_fp8_f32 v197, v191, v192
	v_mul_f32_e32 v193, 0x42800000, v65
	v_mul_f32_e32 v191, 0x42800000, v61
	v_med3_f32 v192, v193, s25, v189
	v_med3_f32 v191, v191, s25, v189
	v_cvt_pk_fp8_f32 v197, v192, v191 op_sel:[0,0,1]
	s_and_b64 vcc, exec, s[2:3]
	ds_write2_b32 v190, v194, v195 offset0:16 offset1:49
	ds_write2_b32 v190, v196, v197 offset0:82 offset1:115
	s_cbranch_vccnz .LBB0_162
	v_add_u32_e32 v50, s27, v172
	v_add_u32_e32 v58, s27, v174
	v_ashrrev_i32_e32 v53, 31, v50
	v_mad_u64_u32 v[50:51], s[16:17], v50, s18, 0
	v_ashrrev_i32_e32 v61, 31, v58
	v_mad_u64_u32 v[58:59], s[30:31], v58, s18, 0
	v_mov_b32_e32 v52, v51
	v_mov_b32_e32 v60, v59
	v_mad_u64_u32 v[52:53], s[16:17], v53, s18, v[52:53]
	v_mad_u64_u32 v[60:61], s[30:31], v61, s18, v[60:61]
	v_mov_b32_e32 v51, v52
	v_add_u32_e32 v52, s27, v173
	v_mov_b32_e32 v59, v60
	v_add_u32_e32 v60, s27, v175
	v_ashrrev_i32_e32 v55, 31, v52
	v_mad_u64_u32 v[52:53], s[30:31], v52, s18, 0
	v_ashrrev_i32_e32 v63, 31, v60
	v_mad_u64_u32 v[60:61], s[30:31], v60, s18, 0
	v_mov_b32_e32 v54, v53
	v_mov_b32_e32 v62, v61
	v_mad_u64_u32 v[54:55], s[30:31], v55, s18, v[54:55]
	v_mad_u64_u32 v[62:63], s[30:31], v63, s18, v[62:63]
	s_ashr_i32 s17, s4, 31
	s_mov_b32 s16, s4
	v_mov_b32_e32 v53, v54
	v_mov_b32_e32 v61, v62
	v_lshl_add_u64 v[50:51], v[50:51], 2, s[8:9]
	s_lshl_b64 s[16:17], s[16:17], 2
	v_lshl_add_u64 v[52:53], v[52:53], 2, s[8:9]
	v_lshl_add_u64 v[58:59], v[58:59], 2, s[8:9]
	v_lshl_add_u64 v[60:61], v[60:61], 2, s[8:9]
	v_lshl_add_u64 v[50:51], v[50:51], 0, s[16:17]
	v_lshl_add_u64 v[52:53], v[52:53], 0, s[16:17]
	v_lshl_add_u64 v[58:59], v[58:59], 0, s[16:17]
	v_lshl_add_u64 v[60:61], v[60:61], 0, s[16:17]
	v_lshl_add_u64 v[50:51], v[50:51], 0, v[134:135]
	v_lshl_add_u64 v[52:53], v[52:53], 0, v[134:135]
	v_lshl_add_u64 v[58:59], v[58:59], 0, v[134:135]
	v_lshl_add_u64 v[60:61], v[60:61], 0, v[134:135]
	global_load_dwordx4 v[54:57], v[50:51], off nt
	s_nop 0
	global_load_dwordx4 v[50:53], v[52:53], off nt
	s_nop 0
	global_load_dwordx4 v[62:65], v[58:59], off nt
	s_nop 0
	global_load_dwordx4 v[58:61], v[60:61], off nt
; #define LAS __attribute__((address_space(3)))
; DI unsigned pk4_fp8(float a, float b, float c, float d) { unsigned p = 0u; p = __builtin_amdgcn_cvt_pk_fp8_f32(f8clamp(a), f8clamp(b), p, false); p = __builtin_amdgcn_cvt_pk_fp8_f32(f8clamp(c), f8clamp(d), p, true); return p; }
; DI void f8_convert_reload(f32x4 (&v)[4][4], int hb, float sc, LAS unsigned char* scr, bool reload, const F8Tile& dn, int lane) {
;     const int nq = lane & 15, kq = lane >> 4;
; #pragma unroll
;     for (int it = 0; it < 4; ++it) {
; #pragma unroll
;         for (int i = 0; i < 4; ++i) *(LAS unsigned*)(scr + (4 * nq + i) * 132 + hb * 64 + it * 16 + kq * 4) = pk4_fp8(v[it][0][i] * sc, v[it][1][i] * sc, v[it][2][i] * sc, v[it][3][i] * sc);
;         if (reload) {
; #pragma unroll
;             for (int j = 0; j < 4; ++j) v[it][j] = __builtin_nontemporal_load((const f32x4*)(dn.W + (size_t)(dn.k0 + hb * 64 + it * 16 + kq * 4 + j) * dn.N + dn.n0 + 4 * nq)); } }
; }
.LBB0_162:
	s_waitcnt vmcnt(28)
	v_mul_f32_e32 v191, 0x42800000, v38
	v_mul_f32_e32 v192, 0x42800000, v34
	v_med3_f32 v191, v191, s25, v189
	v_med3_f32 v192, v192, s25, v189
	v_mov_b32_e32 v194, 0
	v_cvt_pk_fp8_f32 v194, v191, v192
	v_mul_f32_e32 v193, 0x42800000, v46
	v_mul_f32_e32 v191, 0x42800000, v42
	v_med3_f32 v192, v193, s25, v189
	v_med3_f32 v191, v191, s25, v189
	v_cvt_pk_fp8_f32 v194, v192, v191 op_sel:[0,0,1]
	v_mul_f32_e32 v191, 0x42800000, v39
	v_mul_f32_e32 v192, 0x42800000, v35
	v_med3_f32 v191, v191, s25, v189
	v_med3_f32 v192, v192, s25, v189
	v_mov_b32_e32 v195, 0
	v_cvt_pk_fp8_f32 v195, v191, v192
	v_mul_f32_e32 v193, 0x42800000, v47
	v_mul_f32_e32 v191, 0x42800000, v43
	v_med3_f32 v192, v193, s25, v189
	v_med3_f32 v191, v191, s25, v189
	v_cvt_pk_fp8_f32 v195, v192, v191 op_sel:[0,0,1]
	v_mul_f32_e32 v191, 0x42800000, v40
	v_mul_f32_e32 v192, 0x42800000, v36
	v_med3_f32 v191, v191, s25, v189
	v_med3_f32 v192, v192, s25, v189
	v_mov_b32_e32 v196, 0
	v_cvt_pk_fp8_f32 v196, v191, v192
	v_mul_f32_e32 v193, 0x42800000, v48
	v_mul_f32_e32 v191, 0x42800000, v44
	v_med3_f32 v192, v193, s25, v189
	v_med3_f32 v191, v191, s25, v189
	v_cvt_pk_fp8_f32 v196, v192, v191 op_sel:[0,0,1]
	v_mul_f32_e32 v191, 0x42800000, v41
	v_mul_f32_e32 v192, 0x42800000, v37
	v_med3_f32 v191, v191, s25, v189
	v_med3_f32 v192, v192, s25, v189
	v_mov_b32_e32 v197, 0
	v_cvt_pk_fp8_f32 v197, v191, v192
	v_mul_f32_e32 v193, 0x42800000, v49
	v_mul_f32_e32 v191, 0x42800000, v45
	v_med3_f32 v192, v193, s25, v189
	v_med3_f32 v191, v191, s25, v189
	v_cvt_pk_fp8_f32 v197, v192, v191 op_sel:[0,0,1]
	s_and_b64 vcc, exec, s[2:3]
	ds_write2_b32 v190, v194, v195 offset0:20 offset1:53
	ds_write2_b32 v190, v196, v197 offset0:86 offset1:119
	s_cbranch_vccnz .LBB0_164
	v_add_u32_e32 v34, s27, v176
	v_add_u32_e32 v42, s27, v178
	v_ashrrev_i32_e32 v37, 31, v34
	v_mad_u64_u32 v[34:35], s[16:17], v34, s18, 0
	v_ashrrev_i32_e32 v45, 31, v42
	v_mad_u64_u32 v[42:43], s[30:31], v42, s18, 0
	v_mov_b32_e32 v36, v35
	v_mov_b32_e32 v44, v43
	v_mad_u64_u32 v[36:37], s[16:17], v37, s18, v[36:37]
	v_mad_u64_u32 v[44:45], s[30:31], v45, s18, v[44:45]
	v_mov_b32_e32 v35, v36
	v_add_u32_e32 v36, s27, v177
	v_mov_b32_e32 v43, v44
	v_add_u32_e32 v44, s27, v179
	v_ashrrev_i32_e32 v39, 31, v36
	v_mad_u64_u32 v[36:37], s[30:31], v36, s18, 0
	v_ashrrev_i32_e32 v47, 31, v44
	v_mad_u64_u32 v[44:45], s[30:31], v44, s18, 0
	v_mov_b32_e32 v38, v37
	v_mov_b32_e32 v46, v45
	v_mad_u64_u32 v[38:39], s[30:31], v39, s18, v[38:39]
	v_mad_u64_u32 v[46:47], s[30:31], v47, s18, v[46:47]
	s_ashr_i32 s17, s4, 31
	s_mov_b32 s16, s4
	v_mov_b32_e32 v37, v38
	v_mov_b32_e32 v45, v46
	v_lshl_add_u64 v[34:35], v[34:35], 2, s[8:9]
	s_lshl_b64 s[16:17], s[16:17], 2
	v_lshl_add_u64 v[36:37], v[36:37], 2, s[8:9]
	v_lshl_add_u64 v[42:43], v[42:43], 2, s[8:9]
	v_lshl_add_u64 v[44:45], v[44:45], 2, s[8:9]
	v_lshl_add_u64 v[34:35], v[34:35], 0, s[16:17]
	v_lshl_add_u64 v[36:37], v[36:37], 0, s[16:17]
	v_lshl_add_u64 v[42:43], v[42:43], 0, s[16:17]
	v_lshl_add_u64 v[44:45], v[44:45], 0, s[16:17]
	v_lshl_add_u64 v[34:35], v[34:35], 0, v[134:135]
	v_lshl_add_u64 v[36:37], v[36:37], 0, v[134:135]
	v_lshl_add_u64 v[42:43], v[42:43], 0, v[134:135]
	v_lshl_add_u64 v[44:45], v[44:45], 0, v[134:135]
	global_load_dwordx4 v[38:41], v[34:35], off nt
	s_nop 0
	global_load_dwordx4 v[34:37], v[36:37], off nt
	s_nop 0
	global_load_dwordx4 v[46:49], v[42:43], off nt
	s_nop 0
	global_load_dwordx4 v[42:45], v[44:45], off nt
; #define LAS __attribute__((address_space(3)))
; DI unsigned pk4_fp8(float a, float b, float c, float d) { unsigned p = 0u; p = __builtin_amdgcn_cvt_pk_fp8_f32(f8clamp(a), f8clamp(b), p, false); p = __builtin_amdgcn_cvt_pk_fp8_f32(f8clamp(c), f8clamp(d), p, true); return p; }
; DI void f8_convert_reload(f32x4 (&v)[4][4], int hb, float sc, LAS unsigned char* scr, bool reload, const F8Tile& dn, int lane) {
;     const int nq = lane & 15, kq = lane >> 4;
; #pragma unroll
;     for (int it = 0; it < 4; ++it) {
; #pragma unroll
;         for (int i = 0; i < 4; ++i) *(LAS unsigned*)(scr + (4 * nq + i) * 132 + hb * 64 + it * 16 + kq * 4) = pk4_fp8(v[it][0][i] * sc, v[it][1][i] * sc, v[it][2][i] * sc, v[it][3][i] * sc);
;         if (reload) {
; #pragma unroll
;             for (int j = 0; j < 4; ++j) v[it][j] = __builtin_nontemporal_load((const f32x4*)(dn.W + (size_t)(dn.k0 + hb * 64 + it * 16 + kq * 4 + j) * dn.N + dn.n0 + 4 * nq)); } }
; }
.LBB0_164:
	s_waitcnt vmcnt(28)
	v_mul_f32_e32 v191, 0x42800000, v22
	v_mul_f32_e32 v192, 0x42800000, v18
	v_med3_f32 v191, v191, s25, v189
	v_med3_f32 v192, v192, s25, v189
	v_mov_b32_e32 v194, 0
	v_cvt_pk_fp8_f32 v194, v191, v192
	v_mul_f32_e32 v193, 0x42800000, v30
	v_mul_f32_e32 v191, 0x42800000, v26
	v_med3_f32 v192, v193, s25, v189
	v_med3_f32 v191, v191, s25, v189
	v_cvt_pk_fp8_f32 v194, v192, v191 op_sel:[0,0,1]
	v_mul_f32_e32 v191, 0x42800000, v23
	v_mul_f32_e32 v192, 0x42800000, v19
	v_med3_f32 v191, v191, s25, v189
	v_med3_f32 v192, v192, s25, v189
	v_mov_b32_e32 v195, 0
	v_cvt_pk_fp8_f32 v195, v191, v192
	v_mul_f32_e32 v193, 0x42800000, v31
	v_mul_f32_e32 v191, 0x42800000, v27
	v_med3_f32 v192, v193, s25, v189
	v_med3_f32 v191, v191, s25, v189
	v_cvt_pk_fp8_f32 v195, v192, v191 op_sel:[0,0,1]
	v_mul_f32_e32 v191, 0x42800000, v24
	v_mul_f32_e32 v192, 0x42800000, v20
	v_med3_f32 v191, v191, s25, v189
	v_med3_f32 v192, v192, s25, v189
	v_mov_b32_e32 v196, 0
	v_cvt_pk_fp8_f32 v196, v191, v192
	v_mul_f32_e32 v193, 0x42800000, v32
	v_mul_f32_e32 v191, 0x42800000, v28
	v_med3_f32 v192, v193, s25, v189
	v_med3_f32 v191, v191, s25, v189
	v_cvt_pk_fp8_f32 v196, v192, v191 op_sel:[0,0,1]
	v_mul_f32_e32 v191, 0x42800000, v25
	v_mul_f32_e32 v192, 0x42800000, v21
	v_med3_f32 v191, v191, s25, v189
	v_med3_f32 v192, v192, s25, v189
	v_mov_b32_e32 v197, 0
	v_cvt_pk_fp8_f32 v197, v191, v192
	v_mul_f32_e32 v193, 0x42800000, v33
	v_mul_f32_e32 v191, 0x42800000, v29
	v_med3_f32 v192, v193, s25, v189
	v_med3_f32 v191, v191, s25, v189
	v_cvt_pk_fp8_f32 v197, v192, v191 op_sel:[0,0,1]
	s_and_b64 vcc, exec, s[2:3]
	ds_write2_b32 v190, v194, v195 offset0:24 offset1:57
	ds_write2_b32 v190, v196, v197 offset0:90 offset1:123
	s_cbranch_vccnz .LBB0_166
	v_add_u32_e32 v18, s27, v180
	v_add_u32_e32 v26, s27, v182
	v_ashrrev_i32_e32 v21, 31, v18
	v_mad_u64_u32 v[18:19], s[16:17], v18, s18, 0
	v_ashrrev_i32_e32 v29, 31, v26
	v_mad_u64_u32 v[26:27], s[30:31], v26, s18, 0
	v_mov_b32_e32 v20, v19
	v_mov_b32_e32 v28, v27
	v_mad_u64_u32 v[20:21], s[16:17], v21, s18, v[20:21]
	v_mad_u64_u32 v[28:29], s[30:31], v29, s18, v[28:29]
	v_mov_b32_e32 v19, v20
	v_add_u32_e32 v20, s27, v181
	v_mov_b32_e32 v27, v28
	v_add_u32_e32 v28, s27, v183
	v_ashrrev_i32_e32 v23, 31, v20
	v_mad_u64_u32 v[20:21], s[30:31], v20, s18, 0
	v_ashrrev_i32_e32 v31, 31, v28
	v_mad_u64_u32 v[28:29], s[30:31], v28, s18, 0
	v_mov_b32_e32 v22, v21
	v_mov_b32_e32 v30, v29
	v_mad_u64_u32 v[22:23], s[30:31], v23, s18, v[22:23]
	v_mad_u64_u32 v[30:31], s[30:31], v31, s18, v[30:31]
	s_ashr_i32 s17, s4, 31
	s_mov_b32 s16, s4
	v_mov_b32_e32 v21, v22
	v_mov_b32_e32 v29, v30
	v_lshl_add_u64 v[18:19], v[18:19], 2, s[8:9]
	s_lshl_b64 s[16:17], s[16:17], 2
	v_lshl_add_u64 v[20:21], v[20:21], 2, s[8:9]
	v_lshl_add_u64 v[26:27], v[26:27], 2, s[8:9]
	v_lshl_add_u64 v[28:29], v[28:29], 2, s[8:9]
	v_lshl_add_u64 v[18:19], v[18:19], 0, s[16:17]
	v_lshl_add_u64 v[20:21], v[20:21], 0, s[16:17]
	v_lshl_add_u64 v[26:27], v[26:27], 0, s[16:17]
	v_lshl_add_u64 v[28:29], v[28:29], 0, s[16:17]
	v_lshl_add_u64 v[18:19], v[18:19], 0, v[134:135]
	v_lshl_add_u64 v[20:21], v[20:21], 0, v[134:135]
	v_lshl_add_u64 v[26:27], v[26:27], 0, v[134:135]
	v_lshl_add_u64 v[28:29], v[28:29], 0, v[134:135]
	global_load_dwordx4 v[22:25], v[18:19], off nt
	s_nop 0
	global_load_dwordx4 v[18:21], v[20:21], off nt
	s_nop 0
	global_load_dwordx4 v[30:33], v[26:27], off nt
	s_nop 0
	global_load_dwordx4 v[26:29], v[28:29], off nt
.LBB0_166:
	s_waitcnt vmcnt(28)
	v_mul_f32_e32 v191, 0x42800000, v6
	v_mul_f32_e32 v192, 0x42800000, v2
	v_med3_f32 v191, v191, s25, v189
	v_med3_f32 v192, v192, s25, v189
	v_mov_b32_e32 v194, 0
	v_cvt_pk_fp8_f32 v194, v191, v192
	v_mul_f32_e32 v193, 0x42800000, v14
	v_mul_f32_e32 v191, 0x42800000, v10
	v_med3_f32 v192, v193, s25, v189
	v_med3_f32 v191, v191, s25, v189
	v_cvt_pk_fp8_f32 v194, v192, v191 op_sel:[0,0,1]
	v_mul_f32_e32 v191, 0x42800000, v7
	v_mul_f32_e32 v192, 0x42800000, v3
	v_med3_f32 v191, v191, s25, v189
	v_med3_f32 v192, v192, s25, v189
	v_mov_b32_e32 v195, 0
	v_cvt_pk_fp8_f32 v195, v191, v192
	v_mul_f32_e32 v193, 0x42800000, v15
	v_mul_f32_e32 v191, 0x42800000, v11
	v_med3_f32 v192, v193, s25, v189
	v_med3_f32 v191, v191, s25, v189
	v_cvt_pk_fp8_f32 v195, v192, v191 op_sel:[0,0,1]
	v_mul_f32_e32 v191, 0x42800000, v8
	v_mul_f32_e32 v192, 0x42800000, v4
	v_med3_f32 v191, v191, s25, v189
	v_med3_f32 v192, v192, s25, v189
	v_mov_b32_e32 v196, 0
	v_cvt_pk_fp8_f32 v196, v191, v192
	v_mul_f32_e32 v193, 0x42800000, v16
	v_mul_f32_e32 v191, 0x42800000, v12
	v_med3_f32 v192, v193, s25, v189
	v_med3_f32 v191, v191, s25, v189
	v_cvt_pk_fp8_f32 v196, v192, v191 op_sel:[0,0,1]
	v_mul_f32_e32 v191, 0x42800000, v9
	v_mul_f32_e32 v192, 0x42800000, v5
	v_med3_f32 v191, v191, s25, v189
	v_med3_f32 v192, v192, s25, v189
	v_mov_b32_e32 v197, 0
	v_cvt_pk_fp8_f32 v197, v191, v192
	v_mul_f32_e32 v193, 0x42800000, v17
	v_mul_f32_e32 v191, 0x42800000, v13
	v_med3_f32 v192, v193, s25, v189
	v_med3_f32 v191, v191, s25, v189
	v_cvt_pk_fp8_f32 v197, v192, v191 op_sel:[0,0,1]
	s_and_b64 vcc, exec, s[2:3]
	ds_write2_b32 v190, v194, v195 offset0:28 offset1:61
	ds_write2_b32 v190, v196, v197 offset0:94 offset1:127
	s_cbranch_vccnz .LBB0_144
	v_add_u32_e32 v2, s27, v184
	v_add_u32_e32 v10, s27, v186
	v_ashrrev_i32_e32 v5, 31, v2
	v_mad_u64_u32 v[2:3], s[2:3], v2, s18, 0
	v_ashrrev_i32_e32 v13, 31, v10
	v_mad_u64_u32 v[10:11], s[16:17], v10, s18, 0
	v_mov_b32_e32 v4, v3
	v_mov_b32_e32 v12, v11
	v_mad_u64_u32 v[4:5], s[2:3], v5, s18, v[4:5]
	v_mad_u64_u32 v[12:13], s[16:17], v13, s18, v[12:13]
	v_mov_b32_e32 v3, v4
	v_add_u32_e32 v4, s27, v185
	v_mov_b32_e32 v11, v12
	v_add_u32_e32 v12, s27, v187
	v_ashrrev_i32_e32 v7, 31, v4
	v_mad_u64_u32 v[4:5], s[16:17], v4, s18, 0
	v_ashrrev_i32_e32 v15, 31, v12
	v_mad_u64_u32 v[12:13], s[16:17], v12, s18, 0
	v_mov_b32_e32 v6, v5
	v_mov_b32_e32 v14, v13
	v_mad_u64_u32 v[6:7], s[16:17], v7, s18, v[6:7]
	v_mad_u64_u32 v[14:15], s[16:17], v15, s18, v[14:15]
	s_ashr_i32 s3, s4, 31
	s_mov_b32 s2, s4
	v_mov_b32_e32 v5, v6
	v_mov_b32_e32 v13, v14
	v_lshl_add_u64 v[2:3], v[2:3], 2, s[8:9]
	s_lshl_b64 s[2:3], s[2:3], 2
	v_lshl_add_u64 v[4:5], v[4:5], 2, s[8:9]
	v_lshl_add_u64 v[10:11], v[10:11], 2, s[8:9]
	v_lshl_add_u64 v[12:13], v[12:13], 2, s[8:9]
	v_lshl_add_u64 v[2:3], v[2:3], 0, s[2:3]
	v_lshl_add_u64 v[4:5], v[4:5], 0, s[2:3]
	v_lshl_add_u64 v[10:11], v[10:11], 0, s[2:3]
	v_lshl_add_u64 v[12:13], v[12:13], 0, s[2:3]
	v_lshl_add_u64 v[2:3], v[2:3], 0, v[134:135]
	v_lshl_add_u64 v[4:5], v[4:5], 0, v[134:135]
	v_lshl_add_u64 v[10:11], v[10:11], 0, v[134:135]
	v_lshl_add_u64 v[12:13], v[12:13], 0, v[134:135]
	global_load_dwordx4 v[6:9], v[2:3], off nt
	s_nop 0
	global_load_dwordx4 v[2:5], v[4:5], off nt
	s_nop 0
	global_load_dwordx4 v[14:17], v[10:11], off nt
	s_nop 0
	global_load_dwordx4 v[10:13], v[12:13], off nt
	s_branch .LBB0_144

; #define LAS __attribute__((address_space(3)))
; DI void f8_load(f32x4 (&v)[4][4], const F8Tile& d, int hb, int lane) {
;     const int nq = lane & 15, kq = lane >> 4;
; #pragma unroll
;     for (int it = 0; it < 4; ++it)
; #pragma unroll
;         for (int j = 0; j < 4; ++j) v[it][j] = __builtin_nontemporal_load((const f32x4*)(d.W + (size_t)(d.k0 + hb * 64 + it * 16 + kq * 4 + j) * d.N + d.n0 + 4 * nq));
; }
; DI void phase_p0(const Args& A, LAS unsigned char* lds, int it0, int it1, int gw, int ngw, int wave, int lane) {
;     ...
;     if (it < it1) {
;         f32x4 ra[4][4], rb[4][4]; LAS unsigned char* sc8 = (LAS unsigned char*)scr;
;         F8Tile d = desc(it);
;         f8_load(ra, d, 0, lane); f8_load(rb, d, 1, lane);
.LBB0_1345:
	v_lshrrev_b32_e32 v2, 2, v146
	v_and_b32_e32 v1, 12, v2
	v_or_b32_e32 v187, 0x72, v1
	v_or_b32_e32 v188, 0x73, v2
	v_mov_b32_e32 v135, 0
	v_or_b32_e32 v159, 3, v2
	v_or_b32_e32 v163, 19, v2
	v_or_b32_e32 v167, 35, v2
	v_or_b32_e32 v172, 51, v2
	v_or_b32_e32 v176, 0x43, v2
	v_or_b32_e32 v180, 0x53, v2
	v_or_b32_e32 v184, 0x63, v2
	v_add_u32_e32 v2, s4, v188
	v_add_u32_e32 v4, s4, v187
	s_mov_b32 s1, 0
	v_lshlrev_b32_e32 v3, 2, v0
	v_mul_u32_u24_e32 v134, s16, v2
	v_mul_u32_u24_e32 v4, s16, v4
	v_mov_b32_e32 v5, v135
	v_and_b32_e32 v132, 60, v3
	v_lshl_add_u64 v[2:3], v[134:135], 2, s[6:7]
	s_lshl_b64 s[2:3], s[0:1], 2
	v_lshl_add_u64 v[4:5], v[4:5], 2, s[6:7]
	v_lshl_add_u64 v[2:3], v[2:3], 0, s[2:3]
	v_lshlrev_b32_e32 v134, 2, v132
	v_lshl_add_u64 v[4:5], v[4:5], 0, s[2:3]
	v_or_b32_e32 v183, 0x62, v1
	v_or_b32_e32 v185, 0x70, v1
	v_or_b32_e32 v186, 0x71, v1
	v_lshl_add_u64 v[2:3], v[2:3], 0, v[134:135]
	v_lshl_add_u64 v[4:5], v[4:5], 0, v[134:135]
	global_load_dwordx4 v[10:13], v[2:3], off nt
	global_load_dwordx4 v[14:17], v[4:5], off nt
	v_add_u32_e32 v2, s4, v186
	v_add_u32_e32 v4, s4, v185
	v_add_u32_e32 v18, s4, v184
	v_add_u32_e32 v20, s4, v183
	v_mul_u32_u24_e32 v2, s16, v2
	v_mov_b32_e32 v3, v135
	v_mul_u32_u24_e32 v4, s16, v4
	v_mov_b32_e32 v5, v135
	v_mul_u32_u24_e32 v18, s16, v18
	v_mov_b32_e32 v19, v135
	v_mul_u32_u24_e32 v20, s16, v20
	v_mov_b32_e32 v21, v135
	v_lshl_add_u64 v[2:3], v[2:3], 2, s[6:7]
	v_lshl_add_u64 v[4:5], v[4:5], 2, s[6:7]
	v_lshl_add_u64 v[18:19], v[18:19], 2, s[6:7]
	v_lshl_add_u64 v[20:21], v[20:21], 2, s[6:7]
	v_lshl_add_u64 v[2:3], v[2:3], 0, s[2:3]
	v_lshl_add_u64 v[4:5], v[4:5], 0, s[2:3]
	v_lshl_add_u64 v[18:19], v[18:19], 0, s[2:3]
	v_lshl_add_u64 v[20:21], v[20:21], 0, s[2:3]
	v_or_b32_e32 v179, 0x52, v1
	v_or_b32_e32 v181, 0x60, v1
	v_or_b32_e32 v182, 0x61, v1
	v_lshl_add_u64 v[2:3], v[2:3], 0, v[134:135]
	v_lshl_add_u64 v[6:7], v[4:5], 0, v[134:135]
	v_lshl_add_u64 v[18:19], v[18:19], 0, v[134:135]
	v_lshl_add_u64 v[20:21], v[20:21], 0, v[134:135]
	global_load_dwordx4 v[2:5], v[2:3], off nt
	s_nop 0
	global_load_dwordx4 v[6:9], v[6:7], off nt
	s_nop 0
	global_load_dwordx4 v[26:29], v[18:19], off nt
	global_load_dwordx4 v[30:33], v[20:21], off nt
	v_add_u32_e32 v18, s4, v182
	v_add_u32_e32 v20, s4, v181
	v_add_u32_e32 v34, s4, v180
	v_add_u32_e32 v36, s4, v179
	v_mul_u32_u24_e32 v18, s16, v18
	v_mov_b32_e32 v19, v135
	v_mul_u32_u24_e32 v20, s16, v20
	v_mov_b32_e32 v21, v135
	v_mul_u32_u24_e32 v34, s16, v34
	v_mov_b32_e32 v35, v135
	v_mul_u32_u24_e32 v36, s16, v36
	v_mov_b32_e32 v37, v135
	v_lshl_add_u64 v[18:19], v[18:19], 2, s[6:7]
	v_lshl_add_u64 v[20:21], v[20:21], 2, s[6:7]
	v_lshl_add_u64 v[34:35], v[34:35], 2, s[6:7]
	v_lshl_add_u64 v[36:37], v[36:37], 2, s[6:7]
	v_lshl_add_u64 v[18:19], v[18:19], 0, s[2:3]
	v_lshl_add_u64 v[20:21], v[20:21], 0, s[2:3]
	v_lshl_add_u64 v[34:35], v[34:35], 0, s[2:3]
	v_lshl_add_u64 v[36:37], v[36:37], 0, s[2:3]
	v_or_b32_e32 v175, 0x42, v1
	v_or_b32_e32 v177, 0x50, v1
	v_or_b32_e32 v178, 0x51, v1
	v_lshl_add_u64 v[18:19], v[18:19], 0, v[134:135]
	v_lshl_add_u64 v[22:23], v[20:21], 0, v[134:135]
	v_lshl_add_u64 v[34:35], v[34:35], 0, v[134:135]
	v_lshl_add_u64 v[36:37], v[36:37], 0, v[134:135]
	global_load_dwordx4 v[18:21], v[18:19], off nt
	s_nop 0
	global_load_dwordx4 v[22:25], v[22:23], off nt
	s_nop 0
	global_load_dwordx4 v[42:45], v[34:35], off nt
	global_load_dwordx4 v[46:49], v[36:37], off nt
	v_add_u32_e32 v34, s4, v178
	v_add_u32_e32 v36, s4, v177
	v_add_u32_e32 v50, s4, v176
	v_add_u32_e32 v52, s4, v175
	v_mul_u32_u24_e32 v34, s16, v34
	v_mov_b32_e32 v35, v135
	v_mul_u32_u24_e32 v36, s16, v36
	v_mov_b32_e32 v37, v135
	v_mul_u32_u24_e32 v50, s16, v50
	v_mov_b32_e32 v51, v135
	v_mul_u32_u24_e32 v52, s16, v52
	v_mov_b32_e32 v53, v135
	v_lshl_add_u64 v[34:35], v[34:35], 2, s[6:7]
	v_lshl_add_u64 v[36:37], v[36:37], 2, s[6:7]
	v_lshl_add_u64 v[50:51], v[50:51], 2, s[6:7]
	v_lshl_add_u64 v[52:53], v[52:53], 2, s[6:7]
	v_lshl_add_u64 v[34:35], v[34:35], 0, s[2:3]
	v_lshl_add_u64 v[36:37], v[36:37], 0, s[2:3]
	v_lshl_add_u64 v[50:51], v[50:51], 0, s[2:3]
	v_lshl_add_u64 v[52:53], v[52:53], 0, s[2:3]
	v_or_b32_e32 v171, 50, v1
	v_or_b32_e32 v173, 64, v1
	v_or_b32_e32 v174, 0x41, v1
	v_lshl_add_u64 v[34:35], v[34:35], 0, v[134:135]
	v_lshl_add_u64 v[38:39], v[36:37], 0, v[134:135]
	v_lshl_add_u64 v[50:51], v[50:51], 0, v[134:135]
	v_lshl_add_u64 v[52:53], v[52:53], 0, v[134:135]
	global_load_dwordx4 v[34:37], v[34:35], off nt
	s_nop 0
	global_load_dwordx4 v[38:41], v[38:39], off nt
	s_nop 0
	global_load_dwordx4 v[58:61], v[50:51], off nt
	global_load_dwordx4 v[62:65], v[52:53], off nt
	v_add_u32_e32 v50, s4, v174
	v_add_u32_e32 v52, s4, v173
	v_add_u32_e32 v66, s4, v172
	v_add_u32_e32 v68, s4, v171
	v_mul_u32_u24_e32 v50, s16, v50
	v_mov_b32_e32 v51, v135
	v_mul_u32_u24_e32 v52, s16, v52
	v_mov_b32_e32 v53, v135
	v_mul_u32_u24_e32 v66, s16, v66
	v_mov_b32_e32 v67, v135
	v_mul_u32_u24_e32 v68, s16, v68
	v_mov_b32_e32 v69, v135
	v_lshl_add_u64 v[50:51], v[50:51], 2, s[6:7]
	v_lshl_add_u64 v[52:53], v[52:53], 2, s[6:7]
	v_lshl_add_u64 v[66:67], v[66:67], 2, s[6:7]
	v_lshl_add_u64 v[68:69], v[68:69], 2, s[6:7]
	v_lshl_add_u64 v[50:51], v[50:51], 0, s[2:3]
	v_lshl_add_u64 v[52:53], v[52:53], 0, s[2:3]
	v_lshl_add_u64 v[66:67], v[66:67], 0, s[2:3]
	v_lshl_add_u64 v[68:69], v[68:69], 0, s[2:3]
	v_or_b32_e32 v166, 34, v1
	v_or_b32_e32 v168, 48, v1
	v_or_b32_e32 v169, 49, v1
	v_lshl_add_u64 v[50:51], v[50:51], 0, v[134:135]
	v_lshl_add_u64 v[54:55], v[52:53], 0, v[134:135]
	v_lshl_add_u64 v[66:67], v[66:67], 0, v[134:135]
; #define LAS __attribute__((address_space(3)))
; DI void f8_load(f32x4 (&v)[4][4], const F8Tile& d, int hb, int lane) {
;     const int nq = lane & 15, kq = lane >> 4;
; #pragma unroll
;     for (int it = 0; it < 4; ++it)
; #pragma unroll
;         for (int j = 0; j < 4; ++j) v[it][j] = __builtin_nontemporal_load((const f32x4*)(d.W + (size_t)(d.k0 + hb * 64 + it * 16 + kq * 4 + j) * d.N + d.n0 + 4 * nq));
; }
; DI void phase_p0(const Args& A, LAS unsigned char* lds, int it0, int it1, int gw, int ngw, int wave, int lane) {
;     ...
;     if (it < it1) {
;         f32x4 ra[4][4], rb[4][4]; LAS unsigned char* sc8 = (LAS unsigned char*)scr;
;         F8Tile d = desc(it);
;         f8_load(ra, d, 0, lane); f8_load(rb, d, 1, lane);
;         for (; it < it1; it += ngw) {
;             const bool vn = it + ngw < it1; F8Tile dn = d; if (vn) dn = desc(it + ngw);
	v_lshl_add_u64 v[68:69], v[68:69], 0, v[134:135]
	global_load_dwordx4 v[50:53], v[50:51], off nt
	s_nop 0
	global_load_dwordx4 v[54:57], v[54:55], off nt
	s_nop 0
	global_load_dwordx4 v[78:81], v[66:67], off nt
	global_load_dwordx4 v[74:77], v[68:69], off nt
	v_add_u32_e32 v66, s4, v169
	v_add_u32_e32 v68, s4, v168
	v_add_u32_e32 v82, s4, v167
	v_add_u32_e32 v84, s4, v166
	v_mul_u32_u24_e32 v66, s16, v66
	v_mov_b32_e32 v67, v135
	v_mul_u32_u24_e32 v68, s16, v68
	v_mov_b32_e32 v69, v135
	v_mul_u32_u24_e32 v82, s16, v82
	v_mov_b32_e32 v83, v135
	v_mul_u32_u24_e32 v84, s16, v84
	v_mov_b32_e32 v85, v135
	v_lshl_add_u64 v[66:67], v[66:67], 2, s[6:7]
	v_lshl_add_u64 v[68:69], v[68:69], 2, s[6:7]
	v_lshl_add_u64 v[82:83], v[82:83], 2, s[6:7]
	v_lshl_add_u64 v[84:85], v[84:85], 2, s[6:7]
	v_lshl_add_u64 v[66:67], v[66:67], 0, s[2:3]
	v_lshl_add_u64 v[68:69], v[68:69], 0, s[2:3]
	v_lshl_add_u64 v[82:83], v[82:83], 0, s[2:3]
	v_lshl_add_u64 v[84:85], v[84:85], 0, s[2:3]
	v_or_b32_e32 v162, 18, v1
	v_or_b32_e32 v164, 32, v1
	v_or_b32_e32 v165, 33, v1
	v_lshl_add_u64 v[66:67], v[66:67], 0, v[134:135]
	v_lshl_add_u64 v[70:71], v[68:69], 0, v[134:135]
	v_lshl_add_u64 v[82:83], v[82:83], 0, v[134:135]
	v_lshl_add_u64 v[84:85], v[84:85], 0, v[134:135]
	global_load_dwordx4 v[66:69], v[66:67], off nt
	s_nop 0
	global_load_dwordx4 v[70:73], v[70:71], off nt
	s_nop 0
	global_load_dwordx4 v[90:93], v[82:83], off nt
	global_load_dwordx4 v[94:97], v[84:85], off nt
	v_add_u32_e32 v82, s4, v165
	v_add_u32_e32 v84, s4, v164
	v_add_u32_e32 v98, s4, v163
	v_add_u32_e32 v100, s4, v162
	v_mul_u32_u24_e32 v82, s16, v82
	v_mov_b32_e32 v83, v135
	v_mul_u32_u24_e32 v84, s16, v84
	v_mov_b32_e32 v85, v135
	v_mul_u32_u24_e32 v98, s16, v98
	v_mov_b32_e32 v99, v135
	v_mul_u32_u24_e32 v100, s16, v100
	v_mov_b32_e32 v101, v135
	v_lshl_add_u64 v[82:83], v[82:83], 2, s[6:7]
	v_lshl_add_u64 v[84:85], v[84:85], 2, s[6:7]
	v_lshl_add_u64 v[98:99], v[98:99], 2, s[6:7]
	v_lshl_add_u64 v[100:101], v[100:101], 2, s[6:7]
	v_lshl_add_u64 v[82:83], v[82:83], 0, s[2:3]
	v_lshl_add_u64 v[84:85], v[84:85], 0, s[2:3]
	v_lshl_add_u64 v[98:99], v[98:99], 0, s[2:3]
	v_lshl_add_u64 v[100:101], v[100:101], 0, s[2:3]
	v_or_b32_e32 v158, 2, v1
	v_or_b32_e32 v160, 16, v1
	v_or_b32_e32 v161, 17, v1
	v_lshl_add_u64 v[82:83], v[82:83], 0, v[134:135]
	v_lshl_add_u64 v[86:87], v[84:85], 0, v[134:135]
	v_lshl_add_u64 v[98:99], v[98:99], 0, v[134:135]
	v_lshl_add_u64 v[100:101], v[100:101], 0, v[134:135]
	global_load_dwordx4 v[82:85], v[82:83], off nt
	s_nop 0
	global_load_dwordx4 v[86:89], v[86:87], off nt
	s_nop 0
	global_load_dwordx4 v[106:109], v[98:99], off nt
	global_load_dwordx4 v[110:113], v[100:101], off nt
	v_add_u32_e32 v98, s4, v161
	v_add_u32_e32 v100, s4, v160
	v_add_u32_e32 v114, s4, v159
	v_add_u32_e32 v116, s4, v158
	v_mul_u32_u24_e32 v98, s16, v98
	v_mov_b32_e32 v99, v135
	v_mul_u32_u24_e32 v100, s16, v100
	v_mov_b32_e32 v101, v135
	v_mul_u32_u24_e32 v114, s16, v114
	v_mov_b32_e32 v115, v135
	v_mul_u32_u24_e32 v116, s16, v116
	v_mov_b32_e32 v117, v135
	v_lshl_add_u64 v[98:99], v[98:99], 2, s[6:7]
	v_lshl_add_u64 v[100:101], v[100:101], 2, s[6:7]
	v_lshl_add_u64 v[114:115], v[114:115], 2, s[6:7]
	v_lshl_add_u64 v[116:117], v[116:117], 2, s[6:7]
	v_lshl_add_u64 v[98:99], v[98:99], 0, s[2:3]
	v_lshl_add_u64 v[100:101], v[100:101], 0, s[2:3]
	v_lshl_add_u64 v[114:115], v[114:115], 0, s[2:3]
	v_lshl_add_u64 v[116:117], v[116:117], 0, s[2:3]
	v_or_b32_e32 v133, 1, v1
	v_lshl_add_u64 v[98:99], v[98:99], 0, v[134:135]
	v_lshl_add_u64 v[102:103], v[100:101], 0, v[134:135]
	v_lshl_add_u64 v[114:115], v[114:115], 0, v[134:135]
	v_lshl_add_u64 v[116:117], v[116:117], 0, v[134:135]
	global_load_dwordx4 v[98:101], v[98:99], off nt
	s_nop 0
	global_load_dwordx4 v[102:105], v[102:103], off nt
	s_nop 0
	global_load_dwordx4 v[122:125], v[114:115], off nt
	global_load_dwordx4 v[126:129], v[116:117], off nt
	v_add_u32_e32 v114, s4, v133
	v_add_u32_e32 v116, s4, v1
	v_mul_u32_u24_e32 v114, s16, v114
	v_mov_b32_e32 v115, v135
	v_mul_u32_u24_e32 v116, s16, v116
	v_mov_b32_e32 v117, v135
	v_lshl_add_u64 v[114:115], v[114:115], 2, s[6:7]
	v_lshl_add_u64 v[116:117], v[116:117], 2, s[6:7]
	v_lshl_add_u64 v[114:115], v[114:115], 0, s[2:3]
	v_lshl_add_u64 v[116:117], v[116:117], 0, s[2:3]
	v_lshl_add_u64 v[114:115], v[114:115], 0, v[134:135]
	v_lshl_add_u64 v[118:119], v[116:117], 0, v[134:135]
	global_load_dwordx4 v[114:117], v[114:115], off nt
	s_nop 0
	global_load_dwordx4 v[118:121], v[118:119], off nt
	v_readlane_b32 s2, v235, 52
	s_mulk_i32 s2, 0x4200
	v_lshlrev_b32_e32 v137, 4, v0
	s_add_i32 s2, s2, 0
	v_and_b32_e32 v138, 0x70, v137
	v_add_u32_e32 v134, s2, v1
	v_lshrrev_b32_e32 v136, 3, v146
	v_add_u32_e32 v157, s2, v138
	s_lshl_b32 s2, s30, 3
	v_readlane_b32 s12, v235, 54
	v_mov_b32_e32 v131, v135
	v_mul_u32_u24_e32 v156, 0x84, v132
	v_mul_u32_u24_e32 v189, 0x84, v136
	v_readlane_b32 s13, v235, 55
	s_sub_i32 s2, s12, s2
	v_mov_b32_e32 v139, v135
	v_mov_b32_e32 v137, v135
	v_or_b32_e32 v140, 8, v136
	v_mov_b32_e32 v141, v135
	v_or_b32_e32 v142, 16, v136
	v_mov_b32_e32 v143, v135
	v_or_b32_e32 v144, 24, v136
	v_mov_b32_e32 v145, v135
	v_or_b32_e32 v148, 32, v136
	v_mov_b32_e32 v149, v135
	v_or_b32_e32 v150, 40, v136
	v_mov_b32_e32 v151, v135
	v_or_b32_e32 v152, 48, v136
	v_mov_b32_e32 v153, v135
	v_or_b32_e32 v154, 56, v136
	v_mov_b32_e32 v155, v135
	s_add_i32 s23, s2, 0x4480
	s_mov_b32 s24, 0xc3e00000
	v_add_u32_e32 v189, v157, v189
	v_mov_b32_e32 v190, 0x43e00000
	v_add_u32_e32 v191, v134, v156
	v_mov_b64_e32 v[156:157], v[130:131]
	s_mov_b32 s17, s22
	s_mov_b64 s[12:13], s[10:11]
	s_waitcnt vmcnt(0)
	s_branch .LBB0_1347

; #define LAS __attribute__((address_space(3)))
; DI unsigned pk4_fp8(float a, float b, float c, float d) { unsigned p = 0u; p = __builtin_amdgcn_cvt_pk_fp8_f32(f8clamp(a), f8clamp(b), p, false); p = __builtin_amdgcn_cvt_pk_fp8_f32(f8clamp(c), f8clamp(d), p, true); return p; }
; DI void f8_convert_reload(f32x4 (&v)[4][4], int hb, float sc, LAS unsigned char* scr, bool reload, const F8Tile& dn, int lane) {
;     const int nq = lane & 15, kq = lane >> 4;
; #pragma unroll
;     for (int it = 0; it < 4; ++it) {
; #pragma unroll
;         for (int i = 0; i < 4; ++i) *(LAS unsigned*)(scr + (4 * nq + i) * 132 + hb * 64 + it * 16 + kq * 4) = pk4_fp8(v[it][0][i] * sc, v[it][1][i] * sc, v[it][2][i] * sc, v[it][3][i] * sc);
;         if (reload) {
; #pragma unroll
;             for (int j = 0; j < 4; ++j) v[it][j] = __builtin_nontemporal_load((const f32x4*)(dn.W + (size_t)(dn.k0 + hb * 64 + it * 16 + kq * 4 + j) * dn.N + dn.n0 + 4 * nq)); } }
; }
.LBB0_1354:
	s_and_b64 vcc, exec, s[14:15]
	s_cbranch_vccnz .Lcvw2
	s_waitcnt vmcnt(0)
.Lcvw2:
	s_waitcnt vmcnt(28)
	v_mul_f32_e32 v134, 0x42800000, v118
	v_mul_f32_e32 v192, 0x42800000, v114
	v_med3_f32 v134, v134, s24, v190
	v_med3_f32 v192, v192, s24, v190
	v_mov_b32_e32 v194, 0
	v_cvt_pk_fp8_f32 v194, v134, v192
	v_mul_f32_e32 v193, 0x42800000, v126
	v_mul_f32_e32 v134, 0x42800000, v122
	v_med3_f32 v192, v193, s24, v190
	v_med3_f32 v134, v134, s24, v190
	v_cvt_pk_fp8_f32 v194, v192, v134 op_sel:[0,0,1]
	v_mul_f32_e32 v134, 0x42800000, v119
	v_mul_f32_e32 v192, 0x42800000, v115
	v_med3_f32 v134, v134, s24, v190
	v_med3_f32 v192, v192, s24, v190
	v_mov_b32_e32 v195, 0
	v_cvt_pk_fp8_f32 v195, v134, v192
	v_mul_f32_e32 v193, 0x42800000, v127
	v_mul_f32_e32 v134, 0x42800000, v123
	v_med3_f32 v192, v193, s24, v190
	v_med3_f32 v134, v134, s24, v190
	v_cvt_pk_fp8_f32 v195, v192, v134 op_sel:[0,0,1]
	v_mul_f32_e32 v134, 0x42800000, v120
	v_mul_f32_e32 v192, 0x42800000, v116
	v_med3_f32 v134, v134, s24, v190
	v_med3_f32 v192, v192, s24, v190
	v_mov_b32_e32 v196, 0
	v_cvt_pk_fp8_f32 v196, v134, v192
	v_mul_f32_e32 v193, 0x42800000, v128
	v_mul_f32_e32 v134, 0x42800000, v124
	v_med3_f32 v192, v193, s24, v190
	v_med3_f32 v134, v134, s24, v190
	v_cvt_pk_fp8_f32 v196, v192, v134 op_sel:[0,0,1]
	v_mul_f32_e32 v134, 0x42800000, v121
	v_mul_f32_e32 v192, 0x42800000, v117
	v_med3_f32 v134, v134, s24, v190
	v_med3_f32 v192, v192, s24, v190
	v_mov_b32_e32 v197, 0
	v_cvt_pk_fp8_f32 v197, v134, v192
	v_mul_f32_e32 v193, 0x42800000, v129
	v_mul_f32_e32 v134, 0x42800000, v125
	v_med3_f32 v192, v193, s24, v190
	v_med3_f32 v134, v134, s24, v190
	v_cvt_pk_fp8_f32 v197, v192, v134 op_sel:[0,0,1]
	v_cndmask_b32_e64 v134, 0, 1, s[14:15]
	v_cmp_ne_u32_e64 s[2:3], 1, v134
	s_andn2_b64 vcc, exec, s[14:15]
	v_lshlrev_b32_e32 v134, 2, v132
	ds_write2_b32 v191, v194, v195 offset1:33
	ds_write2_b32 v191, v196, v197 offset0:66 offset1:99
	s_cbranch_vccnz .LBB0_1356
	v_add_u32_e32 v114, s26, v1
	v_add_u32_e32 v122, s26, v158
	v_ashrrev_i32_e32 v117, 31, v114
	v_mad_u64_u32 v[114:115], s[14:15], v114, s16, 0
	v_ashrrev_i32_e32 v125, 31, v122
	v_mad_u64_u32 v[122:123], s[28:29], v122, s16, 0
	v_mov_b32_e32 v116, v115
	v_mov_b32_e32 v124, v123
	v_mad_u64_u32 v[116:117], s[14:15], v117, s16, v[116:117]
	v_mad_u64_u32 v[124:125], s[28:29], v125, s16, v[124:125]
	v_mov_b32_e32 v115, v116
	v_add_u32_e32 v116, s26, v133
	v_mov_b32_e32 v123, v124
	v_add_u32_e32 v124, s26, v159
	v_ashrrev_i32_e32 v119, 31, v116
	v_mad_u64_u32 v[116:117], s[28:29], v116, s16, 0
	v_ashrrev_i32_e32 v127, 31, v124
	v_mad_u64_u32 v[124:125], s[28:29], v124, s16, 0
	v_mov_b32_e32 v118, v117
	v_mov_b32_e32 v126, v125
	v_mad_u64_u32 v[118:119], s[28:29], v119, s16, v[118:119]
	v_mad_u64_u32 v[126:127], s[28:29], v127, s16, v[126:127]
	s_ashr_i32 s15, s0, 31
	s_mov_b32 s14, s0
	v_mov_b32_e32 v117, v118
	v_mov_b32_e32 v125, v126
	v_lshl_add_u64 v[114:115], v[114:115], 2, s[6:7]
	s_lshl_b64 s[14:15], s[14:15], 2
	v_lshl_add_u64 v[116:117], v[116:117], 2, s[6:7]
	v_lshl_add_u64 v[122:123], v[122:123], 2, s[6:7]
	v_lshl_add_u64 v[124:125], v[124:125], 2, s[6:7]
	v_lshl_add_u64 v[114:115], v[114:115], 0, s[14:15]
	v_lshl_add_u64 v[116:117], v[116:117], 0, s[14:15]
	v_lshl_add_u64 v[122:123], v[122:123], 0, s[14:15]
	v_lshl_add_u64 v[124:125], v[124:125], 0, s[14:15]
	v_lshl_add_u64 v[114:115], v[114:115], 0, v[134:135]
	v_lshl_add_u64 v[116:117], v[116:117], 0, v[134:135]
	v_lshl_add_u64 v[122:123], v[122:123], 0, v[134:135]
	v_lshl_add_u64 v[124:125], v[124:125], 0, v[134:135]
	global_load_dwordx4 v[118:121], v[114:115], off nt
	s_nop 0
	global_load_dwordx4 v[114:117], v[116:117], off nt
	s_nop 0
	global_load_dwordx4 v[126:129], v[122:123], off nt
	s_nop 0
	global_load_dwordx4 v[122:125], v[124:125], off nt
.LBB0_1356:
	s_waitcnt vmcnt(28)
	v_mul_f32_e32 v192, 0x42800000, v102
	v_mul_f32_e32 v193, 0x42800000, v98
	v_med3_f32 v192, v192, s24, v190
	v_med3_f32 v193, v193, s24, v190
	v_mov_b32_e32 v195, 0
	v_cvt_pk_fp8_f32 v195, v192, v193
	v_mul_f32_e32 v194, 0x42800000, v110
	v_mul_f32_e32 v192, 0x42800000, v106
	v_med3_f32 v193, v194, s24, v190
	v_med3_f32 v192, v192, s24, v190
	v_cvt_pk_fp8_f32 v195, v193, v192 op_sel:[0,0,1]
	v_mul_f32_e32 v192, 0x42800000, v103
	v_mul_f32_e32 v193, 0x42800000, v99
	v_med3_f32 v192, v192, s24, v190
	v_med3_f32 v193, v193, s24, v190
	v_mov_b32_e32 v196, 0
	v_cvt_pk_fp8_f32 v196, v192, v193
	v_mul_f32_e32 v194, 0x42800000, v111
	v_mul_f32_e32 v192, 0x42800000, v107
	v_med3_f32 v193, v194, s24, v190
	v_med3_f32 v192, v192, s24, v190
	v_cvt_pk_fp8_f32 v196, v193, v192 op_sel:[0,0,1]
	v_mul_f32_e32 v192, 0x42800000, v104
	v_mul_f32_e32 v193, 0x42800000, v100
	v_med3_f32 v192, v192, s24, v190
	v_med3_f32 v193, v193, s24, v190
	v_mov_b32_e32 v197, 0
	v_cvt_pk_fp8_f32 v197, v192, v193
	v_mul_f32_e32 v194, 0x42800000, v112
	v_mul_f32_e32 v192, 0x42800000, v108
	v_med3_f32 v193, v194, s24, v190
	v_med3_f32 v192, v192, s24, v190
	v_cvt_pk_fp8_f32 v197, v193, v192 op_sel:[0,0,1]
	v_mul_f32_e32 v192, 0x42800000, v105
	v_mul_f32_e32 v193, 0x42800000, v101
	v_med3_f32 v192, v192, s24, v190
	v_med3_f32 v193, v193, s24, v190
	v_mov_b32_e32 v198, 0
	v_cvt_pk_fp8_f32 v198, v192, v193
	v_mul_f32_e32 v194, 0x42800000, v113
	v_mul_f32_e32 v192, 0x42800000, v109
	v_med3_f32 v193, v194, s24, v190
	v_med3_f32 v192, v192, s24, v190
	v_cvt_pk_fp8_f32 v198, v193, v192 op_sel:[0,0,1]
	s_and_b64 vcc, exec, s[2:3]
	ds_write2_b32 v191, v195, v196 offset0:4 offset1:37
	ds_write2_b32 v191, v197, v198 offset0:70 offset1:103
	s_cbranch_vccnz .LBB0_1358
; #define LAS __attribute__((address_space(3)))
; DI unsigned pk4_fp8(float a, float b, float c, float d) { unsigned p = 0u; p = __builtin_amdgcn_cvt_pk_fp8_f32(f8clamp(a), f8clamp(b), p, false); p = __builtin_amdgcn_cvt_pk_fp8_f32(f8clamp(c), f8clamp(d), p, true); return p; }
; DI void f8_convert_reload(f32x4 (&v)[4][4], int hb, float sc, LAS unsigned char* scr, bool reload, const F8Tile& dn, int lane) {
;     const int nq = lane & 15, kq = lane >> 4;
; #pragma unroll
;     for (int it = 0; it < 4; ++it) {
; #pragma unroll
;         for (int i = 0; i < 4; ++i) *(LAS unsigned*)(scr + (4 * nq + i) * 132 + hb * 64 + it * 16 + kq * 4) = pk4_fp8(v[it][0][i] * sc, v[it][1][i] * sc, v[it][2][i] * sc, v[it][3][i] * sc);
;         if (reload) {
; #pragma unroll
;             for (int j = 0; j < 4; ++j) v[it][j] = __builtin_nontemporal_load((const f32x4*)(dn.W + (size_t)(dn.k0 + hb * 64 + it * 16 + kq * 4 + j) * dn.N + dn.n0 + 4 * nq)); } }
; }
	v_add_u32_e32 v98, s26, v160
	v_add_u32_e32 v106, s26, v162
	v_ashrrev_i32_e32 v101, 31, v98
	v_mad_u64_u32 v[98:99], s[14:15], v98, s16, 0
	v_ashrrev_i32_e32 v109, 31, v106
	v_mad_u64_u32 v[106:107], s[28:29], v106, s16, 0
	v_mov_b32_e32 v100, v99
	v_mov_b32_e32 v108, v107
	v_mad_u64_u32 v[100:101], s[14:15], v101, s16, v[100:101]
	v_mad_u64_u32 v[108:109], s[28:29], v109, s16, v[108:109]
	v_mov_b32_e32 v99, v100
	v_add_u32_e32 v100, s26, v161
	v_mov_b32_e32 v107, v108
	v_add_u32_e32 v108, s26, v163
	v_ashrrev_i32_e32 v103, 31, v100
	v_mad_u64_u32 v[100:101], s[28:29], v100, s16, 0
	v_ashrrev_i32_e32 v111, 31, v108
	v_mad_u64_u32 v[108:109], s[28:29], v108, s16, 0
	v_mov_b32_e32 v102, v101
	v_mov_b32_e32 v110, v109
	v_mad_u64_u32 v[102:103], s[28:29], v103, s16, v[102:103]
	v_mad_u64_u32 v[110:111], s[28:29], v111, s16, v[110:111]
	s_ashr_i32 s15, s0, 31
	s_mov_b32 s14, s0
	v_mov_b32_e32 v101, v102
	v_mov_b32_e32 v109, v110
	v_lshl_add_u64 v[98:99], v[98:99], 2, s[6:7]
	s_lshl_b64 s[14:15], s[14:15], 2
	v_lshl_add_u64 v[100:101], v[100:101], 2, s[6:7]
	v_lshl_add_u64 v[106:107], v[106:107], 2, s[6:7]
	v_lshl_add_u64 v[108:109], v[108:109], 2, s[6:7]
	v_lshl_add_u64 v[98:99], v[98:99], 0, s[14:15]
	v_lshl_add_u64 v[100:101], v[100:101], 0, s[14:15]
	v_lshl_add_u64 v[106:107], v[106:107], 0, s[14:15]
	v_lshl_add_u64 v[108:109], v[108:109], 0, s[14:15]
	v_lshl_add_u64 v[98:99], v[98:99], 0, v[134:135]
	v_lshl_add_u64 v[100:101], v[100:101], 0, v[134:135]
	v_lshl_add_u64 v[106:107], v[106:107], 0, v[134:135]
	v_lshl_add_u64 v[108:109], v[108:109], 0, v[134:135]
	global_load_dwordx4 v[102:105], v[98:99], off nt
	s_nop 0
	global_load_dwordx4 v[98:101], v[100:101], off nt
	s_nop 0
	global_load_dwordx4 v[110:113], v[106:107], off nt
	s_nop 0
	global_load_dwordx4 v[106:109], v[108:109], off nt
.LBB0_1358:
	s_waitcnt vmcnt(28)
	v_mul_f32_e32 v192, 0x42800000, v86
	v_mul_f32_e32 v193, 0x42800000, v82
	v_med3_f32 v192, v192, s24, v190
	v_med3_f32 v193, v193, s24, v190
	v_mov_b32_e32 v195, 0
	v_cvt_pk_fp8_f32 v195, v192, v193
	v_mul_f32_e32 v194, 0x42800000, v94
	v_mul_f32_e32 v192, 0x42800000, v90
	v_med3_f32 v193, v194, s24, v190
	v_med3_f32 v192, v192, s24, v190
	v_cvt_pk_fp8_f32 v195, v193, v192 op_sel:[0,0,1]
	v_mul_f32_e32 v192, 0x42800000, v87
	v_mul_f32_e32 v193, 0x42800000, v83
	v_med3_f32 v192, v192, s24, v190
	v_med3_f32 v193, v193, s24, v190
	v_mov_b32_e32 v196, 0
	v_cvt_pk_fp8_f32 v196, v192, v193
	v_mul_f32_e32 v194, 0x42800000, v95
	v_mul_f32_e32 v192, 0x42800000, v91
	v_med3_f32 v193, v194, s24, v190
	v_med3_f32 v192, v192, s24, v190
	v_cvt_pk_fp8_f32 v196, v193, v192 op_sel:[0,0,1]
	v_mul_f32_e32 v192, 0x42800000, v88
	v_mul_f32_e32 v193, 0x42800000, v84
	v_med3_f32 v192, v192, s24, v190
	v_med3_f32 v193, v193, s24, v190
	v_mov_b32_e32 v197, 0
	v_cvt_pk_fp8_f32 v197, v192, v193
	v_mul_f32_e32 v194, 0x42800000, v96
	v_mul_f32_e32 v192, 0x42800000, v92
	v_med3_f32 v193, v194, s24, v190
	v_med3_f32 v192, v192, s24, v190
	v_cvt_pk_fp8_f32 v197, v193, v192 op_sel:[0,0,1]
	v_mul_f32_e32 v192, 0x42800000, v89
	v_mul_f32_e32 v193, 0x42800000, v85
	v_med3_f32 v192, v192, s24, v190
	v_med3_f32 v193, v193, s24, v190
	v_mov_b32_e32 v198, 0
	v_cvt_pk_fp8_f32 v198, v192, v193
	v_mul_f32_e32 v194, 0x42800000, v97
	v_mul_f32_e32 v192, 0x42800000, v93
	v_med3_f32 v193, v194, s24, v190
	v_med3_f32 v192, v192, s24, v190
	v_cvt_pk_fp8_f32 v198, v193, v192 op_sel:[0,0,1]
	s_and_b64 vcc, exec, s[2:3]
	ds_write2_b32 v191, v195, v196 offset0:8 offset1:41
	ds_write2_b32 v191, v197, v198 offset0:74 offset1:107
	s_cbranch_vccnz .LBB0_1360
	v_add_u32_e32 v82, s26, v164
	v_add_u32_e32 v90, s26, v166
	v_ashrrev_i32_e32 v85, 31, v82
	v_mad_u64_u32 v[82:83], s[14:15], v82, s16, 0
	v_ashrrev_i32_e32 v93, 31, v90
	v_mad_u64_u32 v[90:91], s[28:29], v90, s16, 0
	v_mov_b32_e32 v84, v83
	v_mov_b32_e32 v92, v91
	v_mad_u64_u32 v[84:85], s[14:15], v85, s16, v[84:85]
	v_mad_u64_u32 v[92:93], s[28:29], v93, s16, v[92:93]
	v_mov_b32_e32 v83, v84
	v_add_u32_e32 v84, s26, v165
	v_mov_b32_e32 v91, v92
	v_add_u32_e32 v92, s26, v167
	v_ashrrev_i32_e32 v87, 31, v84
	v_mad_u64_u32 v[84:85], s[28:29], v84, s16, 0
	v_ashrrev_i32_e32 v95, 31, v92
	v_mad_u64_u32 v[92:93], s[28:29], v92, s16, 0
	v_mov_b32_e32 v86, v85
	v_mov_b32_e32 v94, v93
	v_mad_u64_u32 v[86:87], s[28:29], v87, s16, v[86:87]
	v_mad_u64_u32 v[94:95], s[28:29], v95, s16, v[94:95]
	s_ashr_i32 s15, s0, 31
	s_mov_b32 s14, s0
	v_mov_b32_e32 v85, v86
	v_mov_b32_e32 v93, v94
	v_lshl_add_u64 v[82:83], v[82:83], 2, s[6:7]
	s_lshl_b64 s[14:15], s[14:15], 2
	v_lshl_add_u64 v[84:85], v[84:85], 2, s[6:7]
	v_lshl_add_u64 v[90:91], v[90:91], 2, s[6:7]
	v_lshl_add_u64 v[92:93], v[92:93], 2, s[6:7]
	v_lshl_add_u64 v[82:83], v[82:83], 0, s[14:15]
	v_lshl_add_u64 v[84:85], v[84:85], 0, s[14:15]
	v_lshl_add_u64 v[90:91], v[90:91], 0, s[14:15]
	v_lshl_add_u64 v[92:93], v[92:93], 0, s[14:15]
	v_lshl_add_u64 v[82:83], v[82:83], 0, v[134:135]
	v_lshl_add_u64 v[84:85], v[84:85], 0, v[134:135]
	v_lshl_add_u64 v[90:91], v[90:91], 0, v[134:135]
	v_lshl_add_u64 v[92:93], v[92:93], 0, v[134:135]
	global_load_dwordx4 v[86:89], v[82:83], off nt
	s_nop 0
	global_load_dwordx4 v[82:85], v[84:85], off nt
	s_nop 0
	global_load_dwordx4 v[94:97], v[90:91], off nt
	s_nop 0
	global_load_dwordx4 v[90:93], v[92:93], off nt
; #define LAS __attribute__((address_space(3)))
; DI unsigned pk4_fp8(float a, float b, float c, float d) { unsigned p = 0u; p = __builtin_amdgcn_cvt_pk_fp8_f32(f8clamp(a), f8clamp(b), p, false); p = __builtin_amdgcn_cvt_pk_fp8_f32(f8clamp(c), f8clamp(d), p, true); return p; }
; DI void f8_convert_reload(f32x4 (&v)[4][4], int hb, float sc, LAS unsigned char* scr, bool reload, const F8Tile& dn, int lane) {
;     const int nq = lane & 15, kq = lane >> 4;
; #pragma unroll
;     for (int it = 0; it < 4; ++it) {
; #pragma unroll
;         for (int i = 0; i < 4; ++i) *(LAS unsigned*)(scr + (4 * nq + i) * 132 + hb * 64 + it * 16 + kq * 4) = pk4_fp8(v[it][0][i] * sc, v[it][1][i] * sc, v[it][2][i] * sc, v[it][3][i] * sc);
;         if (reload) {
; #pragma unroll
;             for (int j = 0; j < 4; ++j) v[it][j] = __builtin_nontemporal_load((const f32x4*)(dn.W + (size_t)(dn.k0 + hb * 64 + it * 16 + kq * 4 + j) * dn.N + dn.n0 + 4 * nq)); } }
; }
.LBB0_1360:
	s_waitcnt vmcnt(28)
	v_mul_f32_e32 v192, 0x42800000, v70
	v_mul_f32_e32 v193, 0x42800000, v66
	v_med3_f32 v192, v192, s24, v190
	v_med3_f32 v193, v193, s24, v190
	v_mov_b32_e32 v195, 0
	v_cvt_pk_fp8_f32 v195, v192, v193
	v_mul_f32_e32 v194, 0x42800000, v74
	v_mul_f32_e32 v192, 0x42800000, v78
	v_med3_f32 v193, v194, s24, v190
	v_med3_f32 v192, v192, s24, v190
	v_cvt_pk_fp8_f32 v195, v193, v192 op_sel:[0,0,1]
	v_mul_f32_e32 v192, 0x42800000, v71
	v_mul_f32_e32 v193, 0x42800000, v67
	v_med3_f32 v192, v192, s24, v190
	v_med3_f32 v193, v193, s24, v190
	v_mov_b32_e32 v196, 0
	v_cvt_pk_fp8_f32 v196, v192, v193
	v_mul_f32_e32 v194, 0x42800000, v75
	v_mul_f32_e32 v192, 0x42800000, v79
	v_med3_f32 v193, v194, s24, v190
	v_med3_f32 v192, v192, s24, v190
	v_cvt_pk_fp8_f32 v196, v193, v192 op_sel:[0,0,1]
	v_mul_f32_e32 v192, 0x42800000, v72
	v_mul_f32_e32 v193, 0x42800000, v68
	v_med3_f32 v192, v192, s24, v190
	v_med3_f32 v193, v193, s24, v190
	v_mov_b32_e32 v197, 0
	v_cvt_pk_fp8_f32 v197, v192, v193
	v_mul_f32_e32 v194, 0x42800000, v76
	v_mul_f32_e32 v192, 0x42800000, v80
	v_med3_f32 v193, v194, s24, v190
	v_med3_f32 v192, v192, s24, v190
	v_cvt_pk_fp8_f32 v197, v193, v192 op_sel:[0,0,1]
	v_mul_f32_e32 v192, 0x42800000, v73
	v_mul_f32_e32 v193, 0x42800000, v69
	v_med3_f32 v192, v192, s24, v190
	v_med3_f32 v193, v193, s24, v190
	v_mov_b32_e32 v198, 0
	v_cvt_pk_fp8_f32 v198, v192, v193
	v_mul_f32_e32 v194, 0x42800000, v77
	v_mul_f32_e32 v192, 0x42800000, v81
	v_med3_f32 v193, v194, s24, v190
	v_med3_f32 v192, v192, s24, v190
	v_cvt_pk_fp8_f32 v198, v193, v192 op_sel:[0,0,1]
	s_and_b64 vcc, exec, s[2:3]
	ds_write2_b32 v191, v195, v196 offset0:12 offset1:45
	ds_write2_b32 v191, v197, v198 offset0:78 offset1:111
	s_cbranch_vccnz .LBB0_1362
	v_add_u32_e32 v66, s26, v168
	v_add_u32_e32 v74, s26, v171
	v_ashrrev_i32_e32 v69, 31, v66
	v_mad_u64_u32 v[66:67], s[14:15], v66, s16, 0
	v_ashrrev_i32_e32 v77, 31, v74
	v_mad_u64_u32 v[74:75], s[28:29], v74, s16, 0
	v_mov_b32_e32 v68, v67
	v_mov_b32_e32 v76, v75
	v_mad_u64_u32 v[68:69], s[14:15], v69, s16, v[68:69]
	v_mad_u64_u32 v[76:77], s[28:29], v77, s16, v[76:77]
	v_mov_b32_e32 v67, v68
	v_add_u32_e32 v68, s26, v169
	v_mov_b32_e32 v75, v76
	v_add_u32_e32 v76, s26, v172
	v_ashrrev_i32_e32 v71, 31, v68
	v_mad_u64_u32 v[68:69], s[28:29], v68, s16, 0
	v_ashrrev_i32_e32 v79, 31, v76
	v_mad_u64_u32 v[76:77], s[28:29], v76, s16, 0
	v_mov_b32_e32 v70, v69
	v_mov_b32_e32 v78, v77
	v_mad_u64_u32 v[70:71], s[28:29], v71, s16, v[70:71]
	v_mad_u64_u32 v[78:79], s[28:29], v79, s16, v[78:79]
	s_ashr_i32 s15, s0, 31
	s_mov_b32 s14, s0
	v_mov_b32_e32 v69, v70
	v_mov_b32_e32 v77, v78
	v_lshl_add_u64 v[66:67], v[66:67], 2, s[6:7]
	s_lshl_b64 s[14:15], s[14:15], 2
	v_lshl_add_u64 v[68:69], v[68:69], 2, s[6:7]
	v_lshl_add_u64 v[74:75], v[74:75], 2, s[6:7]
	v_lshl_add_u64 v[76:77], v[76:77], 2, s[6:7]
	v_lshl_add_u64 v[66:67], v[66:67], 0, s[14:15]
	v_lshl_add_u64 v[68:69], v[68:69], 0, s[14:15]
	v_lshl_add_u64 v[74:75], v[74:75], 0, s[14:15]
	v_lshl_add_u64 v[76:77], v[76:77], 0, s[14:15]
	v_lshl_add_u64 v[66:67], v[66:67], 0, v[134:135]
	v_lshl_add_u64 v[68:69], v[68:69], 0, v[134:135]
	v_lshl_add_u64 v[74:75], v[74:75], 0, v[134:135]
	v_lshl_add_u64 v[78:79], v[76:77], 0, v[134:135]
	global_load_dwordx4 v[70:73], v[66:67], off nt
	s_nop 0
	global_load_dwordx4 v[66:69], v[68:69], off nt
	s_nop 0
	global_load_dwordx4 v[74:77], v[74:75], off nt
	s_nop 0
	global_load_dwordx4 v[78:81], v[78:79], off nt
.LBB0_1362:
	s_waitcnt vmcnt(28)
	v_mul_f32_e32 v192, 0x42800000, v54
	v_mul_f32_e32 v193, 0x42800000, v50
	v_med3_f32 v192, v192, s24, v190
	v_med3_f32 v193, v193, s24, v190
	v_mov_b32_e32 v195, 0
	v_cvt_pk_fp8_f32 v195, v192, v193
	v_mul_f32_e32 v194, 0x42800000, v62
	v_mul_f32_e32 v192, 0x42800000, v58
	v_med3_f32 v193, v194, s24, v190
	v_med3_f32 v192, v192, s24, v190
	v_cvt_pk_fp8_f32 v195, v193, v192 op_sel:[0,0,1]
	v_mul_f32_e32 v192, 0x42800000, v55
	v_mul_f32_e32 v193, 0x42800000, v51
	v_med3_f32 v192, v192, s24, v190
	v_med3_f32 v193, v193, s24, v190
	v_mov_b32_e32 v196, 0
	v_cvt_pk_fp8_f32 v196, v192, v193
	v_mul_f32_e32 v194, 0x42800000, v63
	v_mul_f32_e32 v192, 0x42800000, v59
	v_med3_f32 v193, v194, s24, v190
	v_med3_f32 v192, v192, s24, v190
	v_cvt_pk_fp8_f32 v196, v193, v192 op_sel:[0,0,1]
	v_mul_f32_e32 v192, 0x42800000, v56
	v_mul_f32_e32 v193, 0x42800000, v52
	v_med3_f32 v192, v192, s24, v190
	v_med3_f32 v193, v193, s24, v190
	v_mov_b32_e32 v197, 0
	v_cvt_pk_fp8_f32 v197, v192, v193
	v_mul_f32_e32 v194, 0x42800000, v64
	v_mul_f32_e32 v192, 0x42800000, v60
	v_med3_f32 v193, v194, s24, v190
	v_med3_f32 v192, v192, s24, v190
	v_cvt_pk_fp8_f32 v197, v193, v192 op_sel:[0,0,1]
	v_mul_f32_e32 v192, 0x42800000, v57
	v_mul_f32_e32 v193, 0x42800000, v53
	v_med3_f32 v192, v192, s24, v190
	v_med3_f32 v193, v193, s24, v190
	v_mov_b32_e32 v198, 0
	v_cvt_pk_fp8_f32 v198, v192, v193
	v_mul_f32_e32 v194, 0x42800000, v65
	v_mul_f32_e32 v192, 0x42800000, v61
	v_med3_f32 v193, v194, s24, v190
	v_med3_f32 v192, v192, s24, v190
	v_cvt_pk_fp8_f32 v198, v193, v192 op_sel:[0,0,1]
	s_and_b64 vcc, exec, s[2:3]
	ds_write2_b32 v191, v195, v196 offset0:16 offset1:49
	ds_write2_b32 v191, v197, v198 offset0:82 offset1:115
	s_cbranch_vccnz .LBB0_1364
	v_add_u32_e32 v50, s26, v173
	v_add_u32_e32 v58, s26, v175
	v_ashrrev_i32_e32 v53, 31, v50
	v_mad_u64_u32 v[50:51], s[14:15], v50, s16, 0
	v_ashrrev_i32_e32 v61, 31, v58
	v_mad_u64_u32 v[58:59], s[28:29], v58, s16, 0
	v_mov_b32_e32 v52, v51
	v_mov_b32_e32 v60, v59
	v_mad_u64_u32 v[52:53], s[14:15], v53, s16, v[52:53]
	v_mad_u64_u32 v[60:61], s[28:29], v61, s16, v[60:61]
	v_mov_b32_e32 v51, v52
	v_add_u32_e32 v52, s26, v174
	v_mov_b32_e32 v59, v60
	v_add_u32_e32 v60, s26, v176
	v_ashrrev_i32_e32 v55, 31, v52
	v_mad_u64_u32 v[52:53], s[28:29], v52, s16, 0
	v_ashrrev_i32_e32 v63, 31, v60
	v_mad_u64_u32 v[60:61], s[28:29], v60, s16, 0
	v_mov_b32_e32 v54, v53
	v_mov_b32_e32 v62, v61
	v_mad_u64_u32 v[54:55], s[28:29], v55, s16, v[54:55]
	v_mad_u64_u32 v[62:63], s[28:29], v63, s16, v[62:63]
	s_ashr_i32 s15, s0, 31
	s_mov_b32 s14, s0
	v_mov_b32_e32 v53, v54
	v_mov_b32_e32 v61, v62
	v_lshl_add_u64 v[50:51], v[50:51], 2, s[6:7]
	s_lshl_b64 s[14:15], s[14:15], 2
	v_lshl_add_u64 v[52:53], v[52:53], 2, s[6:7]
	v_lshl_add_u64 v[58:59], v[58:59], 2, s[6:7]
	v_lshl_add_u64 v[60:61], v[60:61], 2, s[6:7]
	v_lshl_add_u64 v[50:51], v[50:51], 0, s[14:15]
	v_lshl_add_u64 v[52:53], v[52:53], 0, s[14:15]
	v_lshl_add_u64 v[58:59], v[58:59], 0, s[14:15]
	v_lshl_add_u64 v[60:61], v[60:61], 0, s[14:15]
	v_lshl_add_u64 v[50:51], v[50:51], 0, v[134:135]
	v_lshl_add_u64 v[52:53], v[52:53], 0, v[134:135]
	v_lshl_add_u64 v[58:59], v[58:59], 0, v[134:135]
	v_lshl_add_u64 v[60:61], v[60:61], 0, v[134:135]
	global_load_dwordx4 v[54:57], v[50:51], off nt
	s_nop 0
	global_load_dwordx4 v[50:53], v[52:53], off nt
	s_nop 0
	global_load_dwordx4 v[62:65], v[58:59], off nt
	s_nop 0
	global_load_dwordx4 v[58:61], v[60:61], off nt
; #define LAS __attribute__((address_space(3)))
; DI unsigned pk4_fp8(float a, float b, float c, float d) { unsigned p = 0u; p = __builtin_amdgcn_cvt_pk_fp8_f32(f8clamp(a), f8clamp(b), p, false); p = __builtin_amdgcn_cvt_pk_fp8_f32(f8clamp(c), f8clamp(d), p, true); return p; }
; DI void f8_convert_reload(f32x4 (&v)[4][4], int hb, float sc, LAS unsigned char* scr, bool reload, const F8Tile& dn, int lane) {
;     const int nq = lane & 15, kq = lane >> 4;
; #pragma unroll
;     for (int it = 0; it < 4; ++it) {
; #pragma unroll
;         for (int i = 0; i < 4; ++i) *(LAS unsigned*)(scr + (4 * nq + i) * 132 + hb * 64 + it * 16 + kq * 4) = pk4_fp8(v[it][0][i] * sc, v[it][1][i] * sc, v[it][2][i] * sc, v[it][3][i] * sc);
;         if (reload) {
; #pragma unroll
;             for (int j = 0; j < 4; ++j) v[it][j] = __builtin_nontemporal_load((const f32x4*)(dn.W + (size_t)(dn.k0 + hb * 64 + it * 16 + kq * 4 + j) * dn.N + dn.n0 + 4 * nq)); } }
; }
.LBB0_1364:
	s_waitcnt vmcnt(28)
	v_mul_f32_e32 v192, 0x42800000, v38
	v_mul_f32_e32 v193, 0x42800000, v34
	v_med3_f32 v192, v192, s24, v190
	v_med3_f32 v193, v193, s24, v190
	v_mov_b32_e32 v195, 0
	v_cvt_pk_fp8_f32 v195, v192, v193
	v_mul_f32_e32 v194, 0x42800000, v46
	v_mul_f32_e32 v192, 0x42800000, v42
	v_med3_f32 v193, v194, s24, v190
	v_med3_f32 v192, v192, s24, v190
	v_cvt_pk_fp8_f32 v195, v193, v192 op_sel:[0,0,1]
	v_mul_f32_e32 v192, 0x42800000, v39
	v_mul_f32_e32 v193, 0x42800000, v35
	v_med3_f32 v192, v192, s24, v190
	v_med3_f32 v193, v193, s24, v190
	v_mov_b32_e32 v196, 0
	v_cvt_pk_fp8_f32 v196, v192, v193
	v_mul_f32_e32 v194, 0x42800000, v47
	v_mul_f32_e32 v192, 0x42800000, v43
	v_med3_f32 v193, v194, s24, v190
	v_med3_f32 v192, v192, s24, v190
	v_cvt_pk_fp8_f32 v196, v193, v192 op_sel:[0,0,1]
	v_mul_f32_e32 v192, 0x42800000, v40
	v_mul_f32_e32 v193, 0x42800000, v36
	v_med3_f32 v192, v192, s24, v190
	v_med3_f32 v193, v193, s24, v190
	v_mov_b32_e32 v197, 0
	v_cvt_pk_fp8_f32 v197, v192, v193
	v_mul_f32_e32 v194, 0x42800000, v48
	v_mul_f32_e32 v192, 0x42800000, v44
	v_med3_f32 v193, v194, s24, v190
	v_med3_f32 v192, v192, s24, v190
	v_cvt_pk_fp8_f32 v197, v193, v192 op_sel:[0,0,1]
	v_mul_f32_e32 v192, 0x42800000, v41
	v_mul_f32_e32 v193, 0x42800000, v37
	v_med3_f32 v192, v192, s24, v190
	v_med3_f32 v193, v193, s24, v190
	v_mov_b32_e32 v198, 0
	v_cvt_pk_fp8_f32 v198, v192, v193
	v_mul_f32_e32 v194, 0x42800000, v49
	v_mul_f32_e32 v192, 0x42800000, v45
	v_med3_f32 v193, v194, s24, v190
	v_med3_f32 v192, v192, s24, v190
	v_cvt_pk_fp8_f32 v198, v193, v192 op_sel:[0,0,1]
	s_and_b64 vcc, exec, s[2:3]
	ds_write2_b32 v191, v195, v196 offset0:20 offset1:53
	ds_write2_b32 v191, v197, v198 offset0:86 offset1:119
	s_cbranch_vccnz .LBB0_1366
	v_add_u32_e32 v34, s26, v177
	v_add_u32_e32 v42, s26, v179
	v_ashrrev_i32_e32 v37, 31, v34
	v_mad_u64_u32 v[34:35], s[14:15], v34, s16, 0
	v_ashrrev_i32_e32 v45, 31, v42
	v_mad_u64_u32 v[42:43], s[28:29], v42, s16, 0
	v_mov_b32_e32 v36, v35
	v_mov_b32_e32 v44, v43
	v_mad_u64_u32 v[36:37], s[14:15], v37, s16, v[36:37]
	v_mad_u64_u32 v[44:45], s[28:29], v45, s16, v[44:45]
	v_mov_b32_e32 v35, v36
	v_add_u32_e32 v36, s26, v178
	v_mov_b32_e32 v43, v44
	v_add_u32_e32 v44, s26, v180
	v_ashrrev_i32_e32 v39, 31, v36
	v_mad_u64_u32 v[36:37], s[28:29], v36, s16, 0
	v_ashrrev_i32_e32 v47, 31, v44
	v_mad_u64_u32 v[44:45], s[28:29], v44, s16, 0
	v_mov_b32_e32 v38, v37
	v_mov_b32_e32 v46, v45
	v_mad_u64_u32 v[38:39], s[28:29], v39, s16, v[38:39]
	v_mad_u64_u32 v[46:47], s[28:29], v47, s16, v[46:47]
	s_ashr_i32 s15, s0, 31
	s_mov_b32 s14, s0
	v_mov_b32_e32 v37, v38
	v_mov_b32_e32 v45, v46
	v_lshl_add_u64 v[34:35], v[34:35], 2, s[6:7]
	s_lshl_b64 s[14:15], s[14:15], 2
	v_lshl_add_u64 v[36:37], v[36:37], 2, s[6:7]
	v_lshl_add_u64 v[42:43], v[42:43], 2, s[6:7]
	v_lshl_add_u64 v[44:45], v[44:45], 2, s[6:7]
	v_lshl_add_u64 v[34:35], v[34:35], 0, s[14:15]
	v_lshl_add_u64 v[36:37], v[36:37], 0, s[14:15]
	v_lshl_add_u64 v[42:43], v[42:43], 0, s[14:15]
	v_lshl_add_u64 v[44:45], v[44:45], 0, s[14:15]
	v_lshl_add_u64 v[34:35], v[34:35], 0, v[134:135]
	v_lshl_add_u64 v[36:37], v[36:37], 0, v[134:135]
	v_lshl_add_u64 v[42:43], v[42:43], 0, v[134:135]
	v_lshl_add_u64 v[44:45], v[44:45], 0, v[134:135]
	global_load_dwordx4 v[38:41], v[34:35], off nt
	s_nop 0
	global_load_dwordx4 v[34:37], v[36:37], off nt
	s_nop 0
	global_load_dwordx4 v[46:49], v[42:43], off nt
	s_nop 0
	global_load_dwordx4 v[42:45], v[44:45], off nt
; #define LAS __attribute__((address_space(3)))
; DI unsigned pk4_fp8(float a, float b, float c, float d) { unsigned p = 0u; p = __builtin_amdgcn_cvt_pk_fp8_f32(f8clamp(a), f8clamp(b), p, false); p = __builtin_amdgcn_cvt_pk_fp8_f32(f8clamp(c), f8clamp(d), p, true); return p; }
; DI void f8_convert_reload(f32x4 (&v)[4][4], int hb, float sc, LAS unsigned char* scr, bool reload, const F8Tile& dn, int lane) {
;     const int nq = lane & 15, kq = lane >> 4;
; #pragma unroll
;     for (int it = 0; it < 4; ++it) {
; #pragma unroll
;         for (int i = 0; i < 4; ++i) *(LAS unsigned*)(scr + (4 * nq + i) * 132 + hb * 64 + it * 16 + kq * 4) = pk4_fp8(v[it][0][i] * sc, v[it][1][i] * sc, v[it][2][i] * sc, v[it][3][i] * sc);
;         if (reload) {
; #pragma unroll
;             for (int j = 0; j < 4; ++j) v[it][j] = __builtin_nontemporal_load((const f32x4*)(dn.W + (size_t)(dn.k0 + hb * 64 + it * 16 + kq * 4 + j) * dn.N + dn.n0 + 4 * nq)); } }
; }
.LBB0_1366:
	s_waitcnt vmcnt(28)
	v_mul_f32_e32 v192, 0x42800000, v22
	v_mul_f32_e32 v193, 0x42800000, v18
	v_med3_f32 v192, v192, s24, v190
	v_med3_f32 v193, v193, s24, v190
	v_mov_b32_e32 v195, 0
	v_cvt_pk_fp8_f32 v195, v192, v193
	v_mul_f32_e32 v194, 0x42800000, v30
	v_mul_f32_e32 v192, 0x42800000, v26
	v_med3_f32 v193, v194, s24, v190
	v_med3_f32 v192, v192, s24, v190
	v_cvt_pk_fp8_f32 v195, v193, v192 op_sel:[0,0,1]
	v_mul_f32_e32 v192, 0x42800000, v23
	v_mul_f32_e32 v193, 0x42800000, v19
	v_med3_f32 v192, v192, s24, v190
	v_med3_f32 v193, v193, s24, v190
	v_mov_b32_e32 v196, 0
	v_cvt_pk_fp8_f32 v196, v192, v193
	v_mul_f32_e32 v194, 0x42800000, v31
	v_mul_f32_e32 v192, 0x42800000, v27
	v_med3_f32 v193, v194, s24, v190
	v_med3_f32 v192, v192, s24, v190
	v_cvt_pk_fp8_f32 v196, v193, v192 op_sel:[0,0,1]
	v_mul_f32_e32 v192, 0x42800000, v24
	v_mul_f32_e32 v193, 0x42800000, v20
	v_med3_f32 v192, v192, s24, v190
	v_med3_f32 v193, v193, s24, v190
	v_mov_b32_e32 v197, 0
	v_cvt_pk_fp8_f32 v197, v192, v193
	v_mul_f32_e32 v194, 0x42800000, v32
	v_mul_f32_e32 v192, 0x42800000, v28
	v_med3_f32 v193, v194, s24, v190
	v_med3_f32 v192, v192, s24, v190
	v_cvt_pk_fp8_f32 v197, v193, v192 op_sel:[0,0,1]
	v_mul_f32_e32 v192, 0x42800000, v25
	v_mul_f32_e32 v193, 0x42800000, v21
	v_med3_f32 v192, v192, s24, v190
	v_med3_f32 v193, v193, s24, v190
	v_mov_b32_e32 v198, 0
	v_cvt_pk_fp8_f32 v198, v192, v193
	v_mul_f32_e32 v194, 0x42800000, v33
	v_mul_f32_e32 v192, 0x42800000, v29
	v_med3_f32 v193, v194, s24, v190
	v_med3_f32 v192, v192, s24, v190
	v_cvt_pk_fp8_f32 v198, v193, v192 op_sel:[0,0,1]
	s_and_b64 vcc, exec, s[2:3]
	ds_write2_b32 v191, v195, v196 offset0:24 offset1:57
	ds_write2_b32 v191, v197, v198 offset0:90 offset1:123
	s_cbranch_vccnz .LBB0_1368
	v_add_u32_e32 v18, s26, v181
	v_add_u32_e32 v26, s26, v183
	v_ashrrev_i32_e32 v21, 31, v18
	v_mad_u64_u32 v[18:19], s[14:15], v18, s16, 0
	v_ashrrev_i32_e32 v29, 31, v26
	v_mad_u64_u32 v[26:27], s[28:29], v26, s16, 0
	v_mov_b32_e32 v20, v19
	v_mov_b32_e32 v28, v27
	v_mad_u64_u32 v[20:21], s[14:15], v21, s16, v[20:21]
	v_mad_u64_u32 v[28:29], s[28:29], v29, s16, v[28:29]
	v_mov_b32_e32 v19, v20
	v_add_u32_e32 v20, s26, v182
	v_mov_b32_e32 v27, v28
	v_add_u32_e32 v28, s26, v184
	v_ashrrev_i32_e32 v23, 31, v20
	v_mad_u64_u32 v[20:21], s[28:29], v20, s16, 0
	v_ashrrev_i32_e32 v31, 31, v28
	v_mad_u64_u32 v[28:29], s[28:29], v28, s16, 0
	v_mov_b32_e32 v22, v21
	v_mov_b32_e32 v30, v29
	v_mad_u64_u32 v[22:23], s[28:29], v23, s16, v[22:23]
	v_mad_u64_u32 v[30:31], s[28:29], v31, s16, v[30:31]
	s_ashr_i32 s15, s0, 31
	s_mov_b32 s14, s0
	v_mov_b32_e32 v21, v22
	v_mov_b32_e32 v29, v30
	v_lshl_add_u64 v[18:19], v[18:19], 2, s[6:7]
	s_lshl_b64 s[14:15], s[14:15], 2
	v_lshl_add_u64 v[20:21], v[20:21], 2, s[6:7]
	v_lshl_add_u64 v[26:27], v[26:27], 2, s[6:7]
	v_lshl_add_u64 v[28:29], v[28:29], 2, s[6:7]
	v_lshl_add_u64 v[18:19], v[18:19], 0, s[14:15]
	v_lshl_add_u64 v[20:21], v[20:21], 0, s[14:15]
	v_lshl_add_u64 v[26:27], v[26:27], 0, s[14:15]
	v_lshl_add_u64 v[28:29], v[28:29], 0, s[14:15]
	v_lshl_add_u64 v[18:19], v[18:19], 0, v[134:135]
	v_lshl_add_u64 v[20:21], v[20:21], 0, v[134:135]
	v_lshl_add_u64 v[26:27], v[26:27], 0, v[134:135]
	v_lshl_add_u64 v[28:29], v[28:29], 0, v[134:135]
	global_load_dwordx4 v[22:25], v[18:19], off nt
	s_nop 0
	global_load_dwordx4 v[18:21], v[20:21], off nt
	s_nop 0
	global_load_dwordx4 v[30:33], v[26:27], off nt
	s_nop 0
	global_load_dwordx4 v[26:29], v[28:29], off nt
.LBB0_1368:
	s_waitcnt vmcnt(28)
	v_mul_f32_e32 v192, 0x42800000, v6
	v_mul_f32_e32 v193, 0x42800000, v2
	v_med3_f32 v192, v192, s24, v190
	v_med3_f32 v193, v193, s24, v190
	v_mov_b32_e32 v195, 0
	v_cvt_pk_fp8_f32 v195, v192, v193
	v_mul_f32_e32 v194, 0x42800000, v14
	v_mul_f32_e32 v192, 0x42800000, v10
	v_med3_f32 v193, v194, s24, v190
	v_med3_f32 v192, v192, s24, v190
	v_cvt_pk_fp8_f32 v195, v193, v192 op_sel:[0,0,1]
	v_mul_f32_e32 v192, 0x42800000, v7
	v_mul_f32_e32 v193, 0x42800000, v3
	v_med3_f32 v192, v192, s24, v190
	v_med3_f32 v193, v193, s24, v190
	v_mov_b32_e32 v196, 0
	v_cvt_pk_fp8_f32 v196, v192, v193
	v_mul_f32_e32 v194, 0x42800000, v15
	v_mul_f32_e32 v192, 0x42800000, v11
	v_med3_f32 v193, v194, s24, v190
	v_med3_f32 v192, v192, s24, v190
	v_cvt_pk_fp8_f32 v196, v193, v192 op_sel:[0,0,1]
	v_mul_f32_e32 v192, 0x42800000, v8
	v_mul_f32_e32 v193, 0x42800000, v4
	v_med3_f32 v192, v192, s24, v190
	v_med3_f32 v193, v193, s24, v190
	v_mov_b32_e32 v197, 0
	v_cvt_pk_fp8_f32 v197, v192, v193
	v_mul_f32_e32 v194, 0x42800000, v16
	v_mul_f32_e32 v192, 0x42800000, v12
	v_med3_f32 v193, v194, s24, v190
	v_med3_f32 v192, v192, s24, v190
	v_cvt_pk_fp8_f32 v197, v193, v192 op_sel:[0,0,1]
	v_mul_f32_e32 v192, 0x42800000, v9
	v_mul_f32_e32 v193, 0x42800000, v5
	v_med3_f32 v192, v192, s24, v190
	v_med3_f32 v193, v193, s24, v190
	v_mov_b32_e32 v198, 0
	v_cvt_pk_fp8_f32 v198, v192, v193
	v_mul_f32_e32 v194, 0x42800000, v17
	v_mul_f32_e32 v192, 0x42800000, v13
	v_med3_f32 v193, v194, s24, v190
	v_med3_f32 v192, v192, s24, v190
	v_cvt_pk_fp8_f32 v198, v193, v192 op_sel:[0,0,1]
	s_and_b64 vcc, exec, s[2:3]
	ds_write2_b32 v191, v195, v196 offset0:28 offset1:61
	ds_write2_b32 v191, v197, v198 offset0:94 offset1:127
	s_cbranch_vccnz .LBB0_1346
	v_add_u32_e32 v2, s26, v185
	v_add_u32_e32 v10, s26, v187
	v_ashrrev_i32_e32 v5, 31, v2
	v_mad_u64_u32 v[2:3], s[2:3], v2, s16, 0
	v_ashrrev_i32_e32 v13, 31, v10
	v_mad_u64_u32 v[10:11], s[14:15], v10, s16, 0
	v_mov_b32_e32 v4, v3
	v_mov_b32_e32 v12, v11
	v_mad_u64_u32 v[4:5], s[2:3], v5, s16, v[4:5]
	v_mad_u64_u32 v[12:13], s[14:15], v13, s16, v[12:13]
	v_mov_b32_e32 v3, v4
	v_add_u32_e32 v4, s26, v186
	v_mov_b32_e32 v11, v12
	v_add_u32_e32 v12, s26, v188
	v_ashrrev_i32_e32 v7, 31, v4
	v_mad_u64_u32 v[4:5], s[14:15], v4, s16, 0
	v_ashrrev_i32_e32 v15, 31, v12
	v_mad_u64_u32 v[12:13], s[14:15], v12, s16, 0
	v_mov_b32_e32 v6, v5
	v_mov_b32_e32 v14, v13
	v_mad_u64_u32 v[6:7], s[14:15], v7, s16, v[6:7]
	v_mad_u64_u32 v[14:15], s[14:15], v15, s16, v[14:15]
	s_ashr_i32 s3, s0, 31
	s_mov_b32 s2, s0
	v_mov_b32_e32 v5, v6
	v_mov_b32_e32 v13, v14
	v_lshl_add_u64 v[2:3], v[2:3], 2, s[6:7]
	s_lshl_b64 s[2:3], s[2:3], 2
	v_lshl_add_u64 v[4:5], v[4:5], 2, s[6:7]
	v_lshl_add_u64 v[10:11], v[10:11], 2, s[6:7]
	v_lshl_add_u64 v[12:13], v[12:13], 2, s[6:7]
	v_lshl_add_u64 v[2:3], v[2:3], 0, s[2:3]
	v_lshl_add_u64 v[4:5], v[4:5], 0, s[2:3]
	v_lshl_add_u64 v[10:11], v[10:11], 0, s[2:3]
	v_lshl_add_u64 v[12:13], v[12:13], 0, s[2:3]
	v_lshl_add_u64 v[2:3], v[2:3], 0, v[134:135]
	v_lshl_add_u64 v[4:5], v[4:5], 0, v[134:135]
	v_lshl_add_u64 v[10:11], v[10:11], 0, v[134:135]
	v_lshl_add_u64 v[12:13], v[12:13], 0, v[134:135]
	global_load_dwordx4 v[6:9], v[2:3], off nt
	s_nop 0
	global_load_dwordx4 v[2:5], v[4:5], off nt
	s_nop 0
	global_load_dwordx4 v[14:17], v[10:11], off nt
	s_nop 0
	global_load_dwordx4 v[10:13], v[12:13], off nt
	s_branch .LBB0_1346
